# speedup vs baseline: 1.0253x; 1.0253x over previous
.LBB1_30:
	s_load_dwordx8 s[8:15], s[0:1], 0x10
	s_load_dwordx2 s[16:17], s[0:1], 0x30
	s_bitcmp1_b32 s18, 6
	s_cselect_b32 s24, 0x60, 0
	s_lshr_b32 s4, s18, 1
	s_and_b32 s23, s4, 0x7fffffc0
	v_lshrrev_b32_e32 v98, 5, v1
	s_cmpk_lt_u32 s18, 0x200
	v_and_b32_e32 v1, 31, v0
	v_mov_b32_e32 v2, 0
	s_cselect_b64 s[4:5], -1, 0
	s_cmpk_gt_u32 s18, 0x1ff
	v_mov_b32_e32 v3, 0
	v_mov_b32_e32 v4, 0
	v_mov_b32_e32 v5, 0
	v_mov_b32_e32 v6, 0
	v_mov_b32_e32 v7, 0
	v_mov_b32_e32 v8, 0
	v_mov_b32_e32 v9, 0
	v_mov_b32_e32 v10, 0
	v_mov_b32_e32 v11, 0
	v_mov_b32_e32 v12, 0
	v_mov_b32_e32 v13, 0
	v_mov_b32_e32 v14, 0
	v_mov_b32_e32 v15, 0
	v_mov_b32_e32 v16, 0
	v_mov_b32_e32 v17, 0
	v_mov_b32_e32 v50, 0
	v_mov_b32_e32 v51, 0
	v_mov_b32_e32 v52, 0
	v_mov_b32_e32 v53, 0
	v_mov_b32_e32 v54, 0
	v_mov_b32_e32 v55, 0
	v_mov_b32_e32 v56, 0
	v_mov_b32_e32 v57, 0
	v_mov_b32_e32 v58, 0
	v_mov_b32_e32 v59, 0
	v_mov_b32_e32 v60, 0
	v_mov_b32_e32 v61, 0
	v_mov_b32_e32 v62, 0
	v_mov_b32_e32 v63, 0
	v_mov_b32_e32 v64, 0
	v_mov_b32_e32 v65, 0
	v_mov_b32_e32 v18, 0
	v_mov_b32_e32 v19, 0
	v_mov_b32_e32 v20, 0
	v_mov_b32_e32 v21, 0
	v_mov_b32_e32 v22, 0
	v_mov_b32_e32 v23, 0
	v_mov_b32_e32 v24, 0
	v_mov_b32_e32 v25, 0
	v_mov_b32_e32 v26, 0
	v_mov_b32_e32 v27, 0
	v_mov_b32_e32 v28, 0
	v_mov_b32_e32 v29, 0
	v_mov_b32_e32 v30, 0
	v_mov_b32_e32 v31, 0
	v_mov_b32_e32 v32, 0
	v_mov_b32_e32 v33, 0
	v_mov_b32_e32 v66, 0
	v_mov_b32_e32 v67, 0
	v_mov_b32_e32 v68, 0
	v_mov_b32_e32 v69, 0
	v_mov_b32_e32 v70, 0
	v_mov_b32_e32 v71, 0
	v_mov_b32_e32 v72, 0
	v_mov_b32_e32 v73, 0
	v_mov_b32_e32 v74, 0
	v_mov_b32_e32 v75, 0
	v_mov_b32_e32 v76, 0
	v_mov_b32_e32 v77, 0
	v_mov_b32_e32 v78, 0
	v_mov_b32_e32 v79, 0
	v_mov_b32_e32 v80, 0
	v_mov_b32_e32 v81, 0
	v_mov_b32_e32 v34, 0
	v_mov_b32_e32 v35, 0
	v_mov_b32_e32 v36, 0
	v_mov_b32_e32 v37, 0
	v_mov_b32_e32 v38, 0
	v_mov_b32_e32 v39, 0
	v_mov_b32_e32 v40, 0
	v_mov_b32_e32 v41, 0
	v_mov_b32_e32 v42, 0
	v_mov_b32_e32 v43, 0
	v_mov_b32_e32 v44, 0
	v_mov_b32_e32 v45, 0
	v_mov_b32_e32 v46, 0
	v_mov_b32_e32 v47, 0
	v_mov_b32_e32 v48, 0
	v_mov_b32_e32 v49, 0
	v_mov_b32_e32 v82, 0
	v_mov_b32_e32 v83, 0
	v_mov_b32_e32 v84, 0
	v_mov_b32_e32 v85, 0
	v_mov_b32_e32 v86, 0
	v_mov_b32_e32 v87, 0
	v_mov_b32_e32 v88, 0
	v_mov_b32_e32 v89, 0
	v_mov_b32_e32 v90, 0
	v_mov_b32_e32 v91, 0
	v_mov_b32_e32 v92, 0
	v_mov_b32_e32 v93, 0
	v_mov_b32_e32 v94, 0
	v_mov_b32_e32 v95, 0
	v_mov_b32_e32 v96, 0
	v_mov_b32_e32 v97, 0
	v_or_b32_e32 v99, s24, v1
	v_or_b32_e32 v100, s23, v1
	s_cbranch_scc1 .LBB1_35
	v_bfe_u32 v109, v0, 2, 2
	v_xor_b32_e32 v110, v109, v98
	v_xor_b32_e32 v111, 2, v110
	v_lshlrev_b32_e32 v110, 4, v110
	v_lshlrev_b32_e32 v111, 4, v111
	v_lshl_add_u32 v101, v99, 6, v110
	v_lshl_add_u32 v102, v99, 6, v111
	v_lshl_add_u32 v103, v100, 6, v110
	v_lshl_add_u32 v104, v100, 6, v111
	v_add_u32_e32 v103, 0x3000, v103
	v_add_u32_e32 v104, 0x3000, v104
	v_add_u32_e32 v105, 0xe000, v101
	v_add_u32_e32 v106, 0xe000, v102
	v_add_u32_e32 v107, 0xe000, v103
	v_add_u32_e32 v108, 0xe000, v104
	s_cmp_lt_u32 s2, 64
	s_cbranch_scc1 .Lqkv_cv
	s_barrier
	ds_read_b128 v[124:127], v103
	ds_read_b128 v[112:115], v101
	ds_read_b128 v[128:131], v103 offset:2048
	ds_read_b128 v[116:119], v101 offset:2048
	ds_read_b128 v[120:123], v101 offset:4096
	s_waitcnt lgkmcnt(0)
	v_mfma_f32_32x32x16_f16 v[82:97], v[112:115], v[124:127], v[82:97]
	ds_read_b128 v[144:147], v104
	v_mfma_f32_32x32x16_f16 v[34:49], v[112:115], v[128:131], v[34:49]
	ds_read_b128 v[132:135], v102
	v_mfma_f32_32x32x16_f16 v[66:81], v[116:119], v[124:127], v[66:81]
	ds_read_b128 v[148:151], v104 offset:2048
	v_mfma_f32_32x32x16_f16 v[18:33], v[116:119], v[128:131], v[18:33]
	ds_read_b128 v[136:139], v102 offset:2048
	v_mfma_f32_32x32x16_f16 v[50:65], v[120:123], v[124:127], v[50:65]
	ds_read_b128 v[140:143], v102 offset:4096
	v_mfma_f32_32x32x16_f16 v[2:17], v[120:123], v[128:131], v[2:17]
	s_waitcnt lgkmcnt(0)
	s_barrier
	v_mfma_f32_32x32x16_f16 v[82:97], v[132:135], v[144:147], v[82:97]
	ds_read_b128 v[124:127], v103 offset:28672
	v_mfma_f32_32x32x16_f16 v[34:49], v[132:135], v[148:151], v[34:49]
	ds_read_b128 v[112:115], v101 offset:28672
	v_mfma_f32_32x32x16_f16 v[66:81], v[136:139], v[144:147], v[66:81]
	ds_read_b128 v[128:131], v103 offset:30720
	v_mfma_f32_32x32x16_f16 v[18:33], v[136:139], v[148:151], v[18:33]
	ds_read_b128 v[116:119], v101 offset:30720
	v_mfma_f32_32x32x16_f16 v[50:65], v[140:143], v[144:147], v[50:65]
	ds_read_b128 v[120:123], v101 offset:32768
	v_mfma_f32_32x32x16_f16 v[2:17], v[140:143], v[148:151], v[2:17]
	s_waitcnt lgkmcnt(0)
	v_mfma_f32_32x32x16_f16 v[82:97], v[112:115], v[124:127], v[82:97]
	ds_read_b128 v[144:147], v104 offset:28672
	v_mfma_f32_32x32x16_f16 v[34:49], v[112:115], v[128:131], v[34:49]
	ds_read_b128 v[132:135], v102 offset:28672
	v_mfma_f32_32x32x16_f16 v[66:81], v[116:119], v[124:127], v[66:81]
	ds_read_b128 v[148:151], v104 offset:30720
	v_mfma_f32_32x32x16_f16 v[18:33], v[116:119], v[128:131], v[18:33]
	ds_read_b128 v[136:139], v102 offset:30720
	v_mfma_f32_32x32x16_f16 v[50:65], v[120:123], v[124:127], v[50:65]
	ds_read_b128 v[140:143], v102 offset:32768
	v_mfma_f32_32x32x16_f16 v[2:17], v[120:123], v[128:131], v[2:17]
	s_waitcnt lgkmcnt(0)
	s_barrier
	v_mfma_f32_32x32x16_f16 v[82:97], v[132:135], v[144:147], v[82:97]
	ds_read_b128 v[124:127], v107
	v_mfma_f32_32x32x16_f16 v[34:49], v[132:135], v[148:151], v[34:49]
	ds_read_b128 v[112:115], v105
	v_mfma_f32_32x32x16_f16 v[66:81], v[136:139], v[144:147], v[66:81]
	ds_read_b128 v[128:131], v107 offset:2048
	v_mfma_f32_32x32x16_f16 v[18:33], v[136:139], v[148:151], v[18:33]
	ds_read_b128 v[116:119], v105 offset:2048
	v_mfma_f32_32x32x16_f16 v[50:65], v[140:143], v[144:147], v[50:65]
	ds_read_b128 v[120:123], v105 offset:4096
	v_mfma_f32_32x32x16_f16 v[2:17], v[140:143], v[148:151], v[2:17]
	s_waitcnt lgkmcnt(0)
	v_mfma_f32_32x32x16_f16 v[82:97], v[112:115], v[124:127], v[82:97]
	ds_read_b128 v[144:147], v108
	v_mfma_f32_32x32x16_f16 v[34:49], v[112:115], v[128:131], v[34:49]
	ds_read_b128 v[132:135], v106
	v_mfma_f32_32x32x16_f16 v[66:81], v[116:119], v[124:127], v[66:81]
	ds_read_b128 v[148:151], v108 offset:2048
	v_mfma_f32_32x32x16_f16 v[18:33], v[116:119], v[128:131], v[18:33]
	ds_read_b128 v[136:139], v106 offset:2048
	v_mfma_f32_32x32x16_f16 v[50:65], v[120:123], v[124:127], v[50:65]
	ds_read_b128 v[140:143], v106 offset:4096
	v_mfma_f32_32x32x16_f16 v[2:17], v[120:123], v[128:131], v[2:17]
	s_waitcnt lgkmcnt(0)
	s_barrier
	v_mfma_f32_32x32x16_f16 v[82:97], v[132:135], v[144:147], v[82:97]
	ds_read_b128 v[124:127], v107 offset:28672
	v_mfma_f32_32x32x16_f16 v[34:49], v[132:135], v[148:151], v[34:49]
	ds_read_b128 v[112:115], v105 offset:28672
	v_mfma_f32_32x32x16_f16 v[66:81], v[136:139], v[144:147], v[66:81]
	ds_read_b128 v[128:131], v107 offset:30720
	v_mfma_f32_32x32x16_f16 v[18:33], v[136:139], v[148:151], v[18:33]
	ds_read_b128 v[116:119], v105 offset:30720
	v_mfma_f32_32x32x16_f16 v[50:65], v[140:143], v[144:147], v[50:65]
	ds_read_b128 v[120:123], v105 offset:32768
	v_mfma_f32_32x32x16_f16 v[2:17], v[140:143], v[148:151], v[2:17]
	s_waitcnt lgkmcnt(0)
	v_mfma_f32_32x32x16_f16 v[82:97], v[112:115], v[124:127], v[82:97]
	ds_read_b128 v[144:147], v108 offset:28672
	v_mfma_f32_32x32x16_f16 v[34:49], v[112:115], v[128:131], v[34:49]
	ds_read_b128 v[132:135], v106 offset:28672
	v_mfma_f32_32x32x16_f16 v[66:81], v[116:119], v[124:127], v[66:81]
	ds_read_b128 v[148:151], v108 offset:30720
	v_mfma_f32_32x32x16_f16 v[18:33], v[116:119], v[128:131], v[18:33]
	ds_read_b128 v[136:139], v106 offset:30720
	v_mfma_f32_32x32x16_f16 v[50:65], v[120:123], v[124:127], v[50:65]
	ds_read_b128 v[140:143], v106 offset:32768
	v_mfma_f32_32x32x16_f16 v[2:17], v[120:123], v[128:131], v[2:17]
	s_waitcnt lgkmcnt(0)
	s_barrier
	v_mfma_f32_32x32x16_f16 v[82:97], v[132:135], v[144:147], v[82:97]
	ds_read_b128 v[124:127], v103
	v_mfma_f32_32x32x16_f16 v[34:49], v[132:135], v[148:151], v[34:49]
	ds_read_b128 v[112:115], v101
	v_mfma_f32_32x32x16_f16 v[66:81], v[136:139], v[144:147], v[66:81]
	ds_read_b128 v[128:131], v103 offset:2048
	v_mfma_f32_32x32x16_f16 v[18:33], v[136:139], v[148:151], v[18:33]
	ds_read_b128 v[116:119], v101 offset:2048
	v_mfma_f32_32x32x16_f16 v[50:65], v[140:143], v[144:147], v[50:65]
	ds_read_b128 v[120:123], v101 offset:4096
	v_mfma_f32_32x32x16_f16 v[2:17], v[140:143], v[148:151], v[2:17]
	s_waitcnt lgkmcnt(0)
	v_mfma_f32_32x32x16_f16 v[82:97], v[112:115], v[124:127], v[82:97]
	ds_read_b128 v[144:147], v104
	v_mfma_f32_32x32x16_f16 v[34:49], v[112:115], v[128:131], v[34:49]
	ds_read_b128 v[132:135], v102
	v_mfma_f32_32x32x16_f16 v[66:81], v[116:119], v[124:127], v[66:81]
	ds_read_b128 v[148:151], v104 offset:2048
	v_mfma_f32_32x32x16_f16 v[18:33], v[116:119], v[128:131], v[18:33]
	ds_read_b128 v[136:139], v102 offset:2048
	v_mfma_f32_32x32x16_f16 v[50:65], v[120:123], v[124:127], v[50:65]
	ds_read_b128 v[140:143], v102 offset:4096
	v_mfma_f32_32x32x16_f16 v[2:17], v[120:123], v[128:131], v[2:17]
	s_waitcnt lgkmcnt(0)
	s_barrier
	v_mfma_f32_32x32x16_f16 v[82:97], v[132:135], v[144:147], v[82:97]
	ds_read_b128 v[124:127], v103 offset:28672
	v_mfma_f32_32x32x16_f16 v[34:49], v[132:135], v[148:151], v[34:49]
	ds_read_b128 v[112:115], v101 offset:28672
	v_mfma_f32_32x32x16_f16 v[66:81], v[136:139], v[144:147], v[66:81]
	ds_read_b128 v[128:131], v103 offset:30720
	v_mfma_f32_32x32x16_f16 v[18:33], v[136:139], v[148:151], v[18:33]
	ds_read_b128 v[116:119], v101 offset:30720
	v_mfma_f32_32x32x16_f16 v[50:65], v[140:143], v[144:147], v[50:65]
	ds_read_b128 v[120:123], v101 offset:32768
	v_mfma_f32_32x32x16_f16 v[2:17], v[140:143], v[148:151], v[2:17]
	s_waitcnt lgkmcnt(0)
	v_mfma_f32_32x32x16_f16 v[82:97], v[112:115], v[124:127], v[82:97]
	ds_read_b128 v[144:147], v104 offset:28672
	v_mfma_f32_32x32x16_f16 v[34:49], v[112:115], v[128:131], v[34:49]
	ds_read_b128 v[132:135], v102 offset:28672
	v_mfma_f32_32x32x16_f16 v[66:81], v[116:119], v[124:127], v[66:81]
	ds_read_b128 v[148:151], v104 offset:30720
	v_mfma_f32_32x32x16_f16 v[18:33], v[116:119], v[128:131], v[18:33]
	ds_read_b128 v[136:139], v102 offset:30720
	v_mfma_f32_32x32x16_f16 v[50:65], v[120:123], v[124:127], v[50:65]
	ds_read_b128 v[140:143], v102 offset:32768
	v_mfma_f32_32x32x16_f16 v[2:17], v[120:123], v[128:131], v[2:17]
	s_waitcnt lgkmcnt(0)
	s_barrier
	v_mfma_f32_32x32x16_f16 v[82:97], v[132:135], v[144:147], v[82:97]
	ds_read_b128 v[124:127], v107
	v_mfma_f32_32x32x16_f16 v[34:49], v[132:135], v[148:151], v[34:49]
	ds_read_b128 v[112:115], v105
	v_mfma_f32_32x32x16_f16 v[66:81], v[136:139], v[144:147], v[66:81]
	ds_read_b128 v[128:131], v107 offset:2048
	v_mfma_f32_32x32x16_f16 v[18:33], v[136:139], v[148:151], v[18:33]
	ds_read_b128 v[116:119], v105 offset:2048
	v_mfma_f32_32x32x16_f16 v[50:65], v[140:143], v[144:147], v[50:65]
	ds_read_b128 v[120:123], v105 offset:4096
	v_mfma_f32_32x32x16_f16 v[2:17], v[140:143], v[148:151], v[2:17]
	s_waitcnt lgkmcnt(0)
	v_mfma_f32_32x32x16_f16 v[82:97], v[112:115], v[124:127], v[82:97]
	ds_read_b128 v[144:147], v108
	v_mfma_f32_32x32x16_f16 v[34:49], v[112:115], v[128:131], v[34:49]
	ds_read_b128 v[132:135], v106
	v_mfma_f32_32x32x16_f16 v[66:81], v[116:119], v[124:127], v[66:81]
	ds_read_b128 v[148:151], v108 offset:2048
	v_mfma_f32_32x32x16_f16 v[18:33], v[116:119], v[128:131], v[18:33]
	ds_read_b128 v[136:139], v106 offset:2048
	v_mfma_f32_32x32x16_f16 v[50:65], v[120:123], v[124:127], v[50:65]
	ds_read_b128 v[140:143], v106 offset:4096
	v_mfma_f32_32x32x16_f16 v[2:17], v[120:123], v[128:131], v[2:17]
	s_waitcnt lgkmcnt(0)
	s_barrier
	v_mfma_f32_32x32x16_f16 v[82:97], v[132:135], v[144:147], v[82:97]
	ds_read_b128 v[124:127], v107 offset:28672
	v_mfma_f32_32x32x16_f16 v[34:49], v[132:135], v[148:151], v[34:49]
	ds_read_b128 v[112:115], v105 offset:28672
	v_mfma_f32_32x32x16_f16 v[66:81], v[136:139], v[144:147], v[66:81]
	ds_read_b128 v[128:131], v107 offset:30720
	v_mfma_f32_32x32x16_f16 v[18:33], v[136:139], v[148:151], v[18:33]
	ds_read_b128 v[116:119], v105 offset:30720
	v_mfma_f32_32x32x16_f16 v[50:65], v[140:143], v[144:147], v[50:65]
	ds_read_b128 v[120:123], v105 offset:32768
	v_mfma_f32_32x32x16_f16 v[2:17], v[140:143], v[148:151], v[2:17]
	s_waitcnt lgkmcnt(0)
	v_mfma_f32_32x32x16_f16 v[82:97], v[112:115], v[124:127], v[82:97]
	ds_read_b128 v[144:147], v108 offset:28672
	v_mfma_f32_32x32x16_f16 v[34:49], v[112:115], v[128:131], v[34:49]
	ds_read_b128 v[132:135], v106 offset:28672
	v_mfma_f32_32x32x16_f16 v[66:81], v[116:119], v[124:127], v[66:81]
	ds_read_b128 v[148:151], v108 offset:30720
	v_mfma_f32_32x32x16_f16 v[18:33], v[116:119], v[128:131], v[18:33]
	ds_read_b128 v[136:139], v106 offset:30720
	v_mfma_f32_32x32x16_f16 v[50:65], v[120:123], v[124:127], v[50:65]
	ds_read_b128 v[140:143], v106 offset:32768
	v_mfma_f32_32x32x16_f16 v[2:17], v[120:123], v[128:131], v[2:17]
	s_waitcnt lgkmcnt(0)
	s_barrier
	v_mfma_f32_32x32x16_f16 v[82:97], v[132:135], v[144:147], v[82:97]
	ds_read_b128 v[124:127], v103
	v_mfma_f32_32x32x16_f16 v[34:49], v[132:135], v[148:151], v[34:49]
	ds_read_b128 v[112:115], v101
	v_mfma_f32_32x32x16_f16 v[66:81], v[136:139], v[144:147], v[66:81]
	ds_read_b128 v[128:131], v103 offset:2048
	v_mfma_f32_32x32x16_f16 v[18:33], v[136:139], v[148:151], v[18:33]
	ds_read_b128 v[116:119], v101 offset:2048
	v_mfma_f32_32x32x16_f16 v[50:65], v[140:143], v[144:147], v[50:65]
	ds_read_b128 v[120:123], v101 offset:4096
	v_mfma_f32_32x32x16_f16 v[2:17], v[140:143], v[148:151], v[2:17]
	s_waitcnt lgkmcnt(0)
	v_mfma_f32_32x32x16_f16 v[82:97], v[112:115], v[124:127], v[82:97]
	ds_read_b128 v[144:147], v104
	v_mfma_f32_32x32x16_f16 v[34:49], v[112:115], v[128:131], v[34:49]
	ds_read_b128 v[132:135], v102
	v_mfma_f32_32x32x16_f16 v[66:81], v[116:119], v[124:127], v[66:81]
	ds_read_b128 v[148:151], v104 offset:2048
	v_mfma_f32_32x32x16_f16 v[18:33], v[116:119], v[128:131], v[18:33]
	ds_read_b128 v[136:139], v102 offset:2048
	v_mfma_f32_32x32x16_f16 v[50:65], v[120:123], v[124:127], v[50:65]
	ds_read_b128 v[140:143], v102 offset:4096
	v_mfma_f32_32x32x16_f16 v[2:17], v[120:123], v[128:131], v[2:17]
	s_waitcnt lgkmcnt(0)
	s_barrier
	v_mfma_f32_32x32x16_f16 v[82:97], v[132:135], v[144:147], v[82:97]
	ds_read_b128 v[124:127], v103 offset:28672
	v_mfma_f32_32x32x16_f16 v[34:49], v[132:135], v[148:151], v[34:49]
	ds_read_b128 v[112:115], v101 offset:28672
	v_mfma_f32_32x32x16_f16 v[66:81], v[136:139], v[144:147], v[66:81]
	ds_read_b128 v[128:131], v103 offset:30720
	v_mfma_f32_32x32x16_f16 v[18:33], v[136:139], v[148:151], v[18:33]
	ds_read_b128 v[116:119], v101 offset:30720
	v_mfma_f32_32x32x16_f16 v[50:65], v[140:143], v[144:147], v[50:65]
	ds_read_b128 v[120:123], v101 offset:32768
	v_mfma_f32_32x32x16_f16 v[2:17], v[140:143], v[148:151], v[2:17]
	s_waitcnt lgkmcnt(0)
	v_mfma_f32_32x32x16_f16 v[82:97], v[112:115], v[124:127], v[82:97]
	ds_read_b128 v[144:147], v104 offset:28672
	v_mfma_f32_32x32x16_f16 v[34:49], v[112:115], v[128:131], v[34:49]
	ds_read_b128 v[132:135], v102 offset:28672
	v_mfma_f32_32x32x16_f16 v[66:81], v[116:119], v[124:127], v[66:81]
	ds_read_b128 v[148:151], v104 offset:30720
	v_mfma_f32_32x32x16_f16 v[18:33], v[116:119], v[128:131], v[18:33]
	ds_read_b128 v[136:139], v102 offset:30720
	v_mfma_f32_32x32x16_f16 v[50:65], v[120:123], v[124:127], v[50:65]
	ds_read_b128 v[140:143], v102 offset:32768
	v_mfma_f32_32x32x16_f16 v[2:17], v[120:123], v[128:131], v[2:17]
	s_waitcnt lgkmcnt(0)
	s_barrier
	v_mfma_f32_32x32x16_f16 v[82:97], v[132:135], v[144:147], v[82:97]
	ds_read_b128 v[124:127], v107
	v_mfma_f32_32x32x16_f16 v[34:49], v[132:135], v[148:151], v[34:49]
	ds_read_b128 v[112:115], v105
	v_mfma_f32_32x32x16_f16 v[66:81], v[136:139], v[144:147], v[66:81]
	ds_read_b128 v[128:131], v107 offset:2048
	v_mfma_f32_32x32x16_f16 v[18:33], v[136:139], v[148:151], v[18:33]
	ds_read_b128 v[116:119], v105 offset:2048
	v_mfma_f32_32x32x16_f16 v[50:65], v[140:143], v[144:147], v[50:65]
	ds_read_b128 v[120:123], v105 offset:4096
	v_mfma_f32_32x32x16_f16 v[2:17], v[140:143], v[148:151], v[2:17]
	s_waitcnt lgkmcnt(0)
	v_mfma_f32_32x32x16_f16 v[82:97], v[112:115], v[124:127], v[82:97]
	ds_read_b128 v[144:147], v108
	v_mfma_f32_32x32x16_f16 v[34:49], v[112:115], v[128:131], v[34:49]
	ds_read_b128 v[132:135], v106
	v_mfma_f32_32x32x16_f16 v[66:81], v[116:119], v[124:127], v[66:81]
	ds_read_b128 v[148:151], v108 offset:2048
	v_mfma_f32_32x32x16_f16 v[18:33], v[116:119], v[128:131], v[18:33]
	ds_read_b128 v[136:139], v106 offset:2048
	v_mfma_f32_32x32x16_f16 v[50:65], v[120:123], v[124:127], v[50:65]
	ds_read_b128 v[140:143], v106 offset:4096
	v_mfma_f32_32x32x16_f16 v[2:17], v[120:123], v[128:131], v[2:17]
	s_waitcnt lgkmcnt(0)
	s_barrier
	v_mfma_f32_32x32x16_f16 v[82:97], v[132:135], v[144:147], v[82:97]
	ds_read_b128 v[124:127], v107 offset:28672
	v_mfma_f32_32x32x16_f16 v[34:49], v[132:135], v[148:151], v[34:49]
	ds_read_b128 v[112:115], v105 offset:28672
	v_mfma_f32_32x32x16_f16 v[66:81], v[136:139], v[144:147], v[66:81]
	ds_read_b128 v[128:131], v107 offset:30720
	v_mfma_f32_32x32x16_f16 v[18:33], v[136:139], v[148:151], v[18:33]
	ds_read_b128 v[116:119], v105 offset:30720
	v_mfma_f32_32x32x16_f16 v[50:65], v[140:143], v[144:147], v[50:65]
	ds_read_b128 v[120:123], v105 offset:32768
	v_mfma_f32_32x32x16_f16 v[2:17], v[140:143], v[148:151], v[2:17]
	s_waitcnt lgkmcnt(0)
	v_mfma_f32_32x32x16_f16 v[82:97], v[112:115], v[124:127], v[82:97]
	ds_read_b128 v[144:147], v108 offset:28672
	v_mfma_f32_32x32x16_f16 v[34:49], v[112:115], v[128:131], v[34:49]
	ds_read_b128 v[132:135], v106 offset:28672
	v_mfma_f32_32x32x16_f16 v[66:81], v[116:119], v[124:127], v[66:81]
	ds_read_b128 v[148:151], v108 offset:30720
	v_mfma_f32_32x32x16_f16 v[18:33], v[116:119], v[128:131], v[18:33]
	ds_read_b128 v[136:139], v106 offset:30720
	v_mfma_f32_32x32x16_f16 v[50:65], v[120:123], v[124:127], v[50:65]
	ds_read_b128 v[140:143], v106 offset:32768
	v_mfma_f32_32x32x16_f16 v[2:17], v[120:123], v[128:131], v[2:17]
	s_waitcnt lgkmcnt(0)
	s_barrier
	v_mfma_f32_32x32x16_f16 v[82:97], v[132:135], v[144:147], v[82:97]
	ds_read_b128 v[124:127], v103
	v_mfma_f32_32x32x16_f16 v[34:49], v[132:135], v[148:151], v[34:49]
	ds_read_b128 v[112:115], v101
	v_mfma_f32_32x32x16_f16 v[66:81], v[136:139], v[144:147], v[66:81]
	ds_read_b128 v[128:131], v103 offset:2048
	v_mfma_f32_32x32x16_f16 v[18:33], v[136:139], v[148:151], v[18:33]
	ds_read_b128 v[116:119], v101 offset:2048
	v_mfma_f32_32x32x16_f16 v[50:65], v[140:143], v[144:147], v[50:65]
	ds_read_b128 v[120:123], v101 offset:4096
	v_mfma_f32_32x32x16_f16 v[2:17], v[140:143], v[148:151], v[2:17]
	s_waitcnt lgkmcnt(0)
	v_mfma_f32_32x32x16_f16 v[82:97], v[112:115], v[124:127], v[82:97]
	ds_read_b128 v[144:147], v104
	v_mfma_f32_32x32x16_f16 v[34:49], v[112:115], v[128:131], v[34:49]
	ds_read_b128 v[132:135], v102
	v_mfma_f32_32x32x16_f16 v[66:81], v[116:119], v[124:127], v[66:81]
	ds_read_b128 v[148:151], v104 offset:2048
	v_mfma_f32_32x32x16_f16 v[18:33], v[116:119], v[128:131], v[18:33]
	ds_read_b128 v[136:139], v102 offset:2048
	v_mfma_f32_32x32x16_f16 v[50:65], v[120:123], v[124:127], v[50:65]
	ds_read_b128 v[140:143], v102 offset:4096
	v_mfma_f32_32x32x16_f16 v[2:17], v[120:123], v[128:131], v[2:17]
	s_waitcnt lgkmcnt(0)
	s_barrier
	v_mfma_f32_32x32x16_f16 v[82:97], v[132:135], v[144:147], v[82:97]
	ds_read_b128 v[124:127], v103 offset:28672
	v_mfma_f32_32x32x16_f16 v[34:49], v[132:135], v[148:151], v[34:49]
	ds_read_b128 v[112:115], v101 offset:28672
	v_mfma_f32_32x32x16_f16 v[66:81], v[136:139], v[144:147], v[66:81]
	ds_read_b128 v[128:131], v103 offset:30720
	v_mfma_f32_32x32x16_f16 v[18:33], v[136:139], v[148:151], v[18:33]
	ds_read_b128 v[116:119], v101 offset:30720
	v_mfma_f32_32x32x16_f16 v[50:65], v[140:143], v[144:147], v[50:65]
	ds_read_b128 v[120:123], v101 offset:32768
	v_mfma_f32_32x32x16_f16 v[2:17], v[140:143], v[148:151], v[2:17]
	s_waitcnt lgkmcnt(0)
	v_mfma_f32_32x32x16_f16 v[82:97], v[112:115], v[124:127], v[82:97]
	ds_read_b128 v[144:147], v104 offset:28672
	v_mfma_f32_32x32x16_f16 v[34:49], v[112:115], v[128:131], v[34:49]
	ds_read_b128 v[132:135], v102 offset:28672
	v_mfma_f32_32x32x16_f16 v[66:81], v[116:119], v[124:127], v[66:81]
	ds_read_b128 v[148:151], v104 offset:30720
	v_mfma_f32_32x32x16_f16 v[18:33], v[116:119], v[128:131], v[18:33]
	ds_read_b128 v[136:139], v102 offset:30720
	v_mfma_f32_32x32x16_f16 v[50:65], v[120:123], v[124:127], v[50:65]
	ds_read_b128 v[140:143], v102 offset:32768
	v_mfma_f32_32x32x16_f16 v[2:17], v[120:123], v[128:131], v[2:17]
	s_waitcnt lgkmcnt(0)
	s_barrier
	v_mfma_f32_32x32x16_f16 v[82:97], v[132:135], v[144:147], v[82:97]
	ds_read_b128 v[124:127], v107
	v_mfma_f32_32x32x16_f16 v[34:49], v[132:135], v[148:151], v[34:49]
	ds_read_b128 v[112:115], v105
	v_mfma_f32_32x32x16_f16 v[66:81], v[136:139], v[144:147], v[66:81]
	ds_read_b128 v[128:131], v107 offset:2048
	v_mfma_f32_32x32x16_f16 v[18:33], v[136:139], v[148:151], v[18:33]
	ds_read_b128 v[116:119], v105 offset:2048
	v_mfma_f32_32x32x16_f16 v[50:65], v[140:143], v[144:147], v[50:65]
	ds_read_b128 v[120:123], v105 offset:4096
	v_mfma_f32_32x32x16_f16 v[2:17], v[140:143], v[148:151], v[2:17]
	s_waitcnt lgkmcnt(0)
	v_mfma_f32_32x32x16_f16 v[82:97], v[112:115], v[124:127], v[82:97]
	ds_read_b128 v[144:147], v108
	v_mfma_f32_32x32x16_f16 v[34:49], v[112:115], v[128:131], v[34:49]
	ds_read_b128 v[132:135], v106
	v_mfma_f32_32x32x16_f16 v[66:81], v[116:119], v[124:127], v[66:81]
	ds_read_b128 v[148:151], v108 offset:2048
	v_mfma_f32_32x32x16_f16 v[18:33], v[116:119], v[128:131], v[18:33]
	ds_read_b128 v[136:139], v106 offset:2048
	v_mfma_f32_32x32x16_f16 v[50:65], v[120:123], v[124:127], v[50:65]
	ds_read_b128 v[140:143], v106 offset:4096
	v_mfma_f32_32x32x16_f16 v[2:17], v[120:123], v[128:131], v[2:17]
	s_waitcnt lgkmcnt(0)
	s_barrier
	v_mfma_f32_32x32x16_f16 v[82:97], v[132:135], v[144:147], v[82:97]
	ds_read_b128 v[124:127], v107 offset:28672
	v_mfma_f32_32x32x16_f16 v[34:49], v[132:135], v[148:151], v[34:49]
	ds_read_b128 v[112:115], v105 offset:28672
	v_mfma_f32_32x32x16_f16 v[66:81], v[136:139], v[144:147], v[66:81]
	ds_read_b128 v[128:131], v107 offset:30720
	v_mfma_f32_32x32x16_f16 v[18:33], v[136:139], v[148:151], v[18:33]
	ds_read_b128 v[116:119], v105 offset:30720
	v_mfma_f32_32x32x16_f16 v[50:65], v[140:143], v[144:147], v[50:65]
	ds_read_b128 v[120:123], v105 offset:32768
	v_mfma_f32_32x32x16_f16 v[2:17], v[140:143], v[148:151], v[2:17]
	s_waitcnt lgkmcnt(0)
	v_mfma_f32_32x32x16_f16 v[82:97], v[112:115], v[124:127], v[82:97]
	ds_read_b128 v[144:147], v108 offset:28672
	v_mfma_f32_32x32x16_f16 v[34:49], v[112:115], v[128:131], v[34:49]
	ds_read_b128 v[132:135], v106 offset:28672
	v_mfma_f32_32x32x16_f16 v[66:81], v[116:119], v[124:127], v[66:81]
	ds_read_b128 v[148:151], v108 offset:30720
	v_mfma_f32_32x32x16_f16 v[18:33], v[116:119], v[128:131], v[18:33]
	ds_read_b128 v[136:139], v106 offset:30720
	v_mfma_f32_32x32x16_f16 v[50:65], v[120:123], v[124:127], v[50:65]
	ds_read_b128 v[140:143], v106 offset:32768
	v_mfma_f32_32x32x16_f16 v[2:17], v[120:123], v[128:131], v[2:17]
	s_waitcnt lgkmcnt(0)
	s_barrier
	v_mfma_f32_32x32x16_f16 v[82:97], v[132:135], v[144:147], v[82:97]
	ds_read_b128 v[124:127], v103
	v_mfma_f32_32x32x16_f16 v[34:49], v[132:135], v[148:151], v[34:49]
	ds_read_b128 v[112:115], v101
	v_mfma_f32_32x32x16_f16 v[66:81], v[136:139], v[144:147], v[66:81]
	ds_read_b128 v[128:131], v103 offset:2048
	v_mfma_f32_32x32x16_f16 v[18:33], v[136:139], v[148:151], v[18:33]
	ds_read_b128 v[116:119], v101 offset:2048
	v_mfma_f32_32x32x16_f16 v[50:65], v[140:143], v[144:147], v[50:65]
	ds_read_b128 v[120:123], v101 offset:4096
	v_mfma_f32_32x32x16_f16 v[2:17], v[140:143], v[148:151], v[2:17]
	s_waitcnt lgkmcnt(0)
	v_mfma_f32_32x32x16_f16 v[82:97], v[112:115], v[124:127], v[82:97]
	ds_read_b128 v[144:147], v104
	v_mfma_f32_32x32x16_f16 v[34:49], v[112:115], v[128:131], v[34:49]
	ds_read_b128 v[132:135], v102
	v_mfma_f32_32x32x16_f16 v[66:81], v[116:119], v[124:127], v[66:81]
	ds_read_b128 v[148:151], v104 offset:2048
	v_mfma_f32_32x32x16_f16 v[18:33], v[116:119], v[128:131], v[18:33]
	ds_read_b128 v[136:139], v102 offset:2048
	v_mfma_f32_32x32x16_f16 v[50:65], v[120:123], v[124:127], v[50:65]
	ds_read_b128 v[140:143], v102 offset:4096
	v_mfma_f32_32x32x16_f16 v[2:17], v[120:123], v[128:131], v[2:17]
	s_waitcnt lgkmcnt(0)
	s_barrier
	v_mfma_f32_32x32x16_f16 v[82:97], v[132:135], v[144:147], v[82:97]
	ds_read_b128 v[124:127], v103 offset:28672
	v_mfma_f32_32x32x16_f16 v[34:49], v[132:135], v[148:151], v[34:49]
	ds_read_b128 v[112:115], v101 offset:28672
	v_mfma_f32_32x32x16_f16 v[66:81], v[136:139], v[144:147], v[66:81]
	ds_read_b128 v[128:131], v103 offset:30720
	v_mfma_f32_32x32x16_f16 v[18:33], v[136:139], v[148:151], v[18:33]
	ds_read_b128 v[116:119], v101 offset:30720
	v_mfma_f32_32x32x16_f16 v[50:65], v[140:143], v[144:147], v[50:65]
	ds_read_b128 v[120:123], v101 offset:32768
	v_mfma_f32_32x32x16_f16 v[2:17], v[140:143], v[148:151], v[2:17]
	s_waitcnt lgkmcnt(0)
	v_mfma_f32_32x32x16_f16 v[82:97], v[112:115], v[124:127], v[82:97]
	ds_read_b128 v[144:147], v104 offset:28672
	v_mfma_f32_32x32x16_f16 v[34:49], v[112:115], v[128:131], v[34:49]
	ds_read_b128 v[132:135], v102 offset:28672
	v_mfma_f32_32x32x16_f16 v[66:81], v[116:119], v[124:127], v[66:81]
	ds_read_b128 v[148:151], v104 offset:30720
	v_mfma_f32_32x32x16_f16 v[18:33], v[116:119], v[128:131], v[18:33]
	ds_read_b128 v[136:139], v102 offset:30720
	v_mfma_f32_32x32x16_f16 v[50:65], v[120:123], v[124:127], v[50:65]
	ds_read_b128 v[140:143], v102 offset:32768
	v_mfma_f32_32x32x16_f16 v[2:17], v[120:123], v[128:131], v[2:17]
	s_waitcnt lgkmcnt(0)
	s_barrier
	v_mfma_f32_32x32x16_f16 v[82:97], v[132:135], v[144:147], v[82:97]
	ds_read_b128 v[124:127], v107
	v_mfma_f32_32x32x16_f16 v[34:49], v[132:135], v[148:151], v[34:49]
	ds_read_b128 v[112:115], v105
	v_mfma_f32_32x32x16_f16 v[66:81], v[136:139], v[144:147], v[66:81]
	ds_read_b128 v[128:131], v107 offset:2048
	v_mfma_f32_32x32x16_f16 v[18:33], v[136:139], v[148:151], v[18:33]
	ds_read_b128 v[116:119], v105 offset:2048
	v_mfma_f32_32x32x16_f16 v[50:65], v[140:143], v[144:147], v[50:65]
	ds_read_b128 v[120:123], v105 offset:4096
	v_mfma_f32_32x32x16_f16 v[2:17], v[140:143], v[148:151], v[2:17]
	s_waitcnt lgkmcnt(0)
	v_mfma_f32_32x32x16_f16 v[82:97], v[112:115], v[124:127], v[82:97]
	ds_read_b128 v[144:147], v108
	v_mfma_f32_32x32x16_f16 v[34:49], v[112:115], v[128:131], v[34:49]
	ds_read_b128 v[132:135], v106
	v_mfma_f32_32x32x16_f16 v[66:81], v[116:119], v[124:127], v[66:81]
	ds_read_b128 v[148:151], v108 offset:2048
	v_mfma_f32_32x32x16_f16 v[18:33], v[116:119], v[128:131], v[18:33]
	ds_read_b128 v[136:139], v106 offset:2048
	v_mfma_f32_32x32x16_f16 v[50:65], v[120:123], v[124:127], v[50:65]
	ds_read_b128 v[140:143], v106 offset:4096
	v_mfma_f32_32x32x16_f16 v[2:17], v[120:123], v[128:131], v[2:17]
	s_waitcnt lgkmcnt(0)
	s_barrier
	v_mfma_f32_32x32x16_f16 v[82:97], v[132:135], v[144:147], v[82:97]
	ds_read_b128 v[124:127], v107 offset:28672
	v_mfma_f32_32x32x16_f16 v[34:49], v[132:135], v[148:151], v[34:49]
	ds_read_b128 v[112:115], v105 offset:28672
	v_mfma_f32_32x32x16_f16 v[66:81], v[136:139], v[144:147], v[66:81]
	ds_read_b128 v[128:131], v107 offset:30720
	v_mfma_f32_32x32x16_f16 v[18:33], v[136:139], v[148:151], v[18:33]
	ds_read_b128 v[116:119], v105 offset:30720
	v_mfma_f32_32x32x16_f16 v[50:65], v[140:143], v[144:147], v[50:65]
	ds_read_b128 v[120:123], v105 offset:32768
	v_mfma_f32_32x32x16_f16 v[2:17], v[140:143], v[148:151], v[2:17]
	s_waitcnt lgkmcnt(0)
	v_mfma_f32_32x32x16_f16 v[82:97], v[112:115], v[124:127], v[82:97]
	ds_read_b128 v[144:147], v108 offset:28672
	v_mfma_f32_32x32x16_f16 v[34:49], v[112:115], v[128:131], v[34:49]
	ds_read_b128 v[132:135], v106 offset:28672
	v_mfma_f32_32x32x16_f16 v[66:81], v[116:119], v[124:127], v[66:81]
	ds_read_b128 v[148:151], v108 offset:30720
	v_mfma_f32_32x32x16_f16 v[18:33], v[116:119], v[128:131], v[18:33]
	ds_read_b128 v[136:139], v106 offset:30720
	v_mfma_f32_32x32x16_f16 v[50:65], v[120:123], v[124:127], v[50:65]
	ds_read_b128 v[140:143], v106 offset:32768
	v_mfma_f32_32x32x16_f16 v[2:17], v[120:123], v[128:131], v[2:17]
	s_waitcnt lgkmcnt(0)
	s_barrier
	v_mfma_f32_32x32x16_f16 v[82:97], v[132:135], v[144:147], v[82:97]
	ds_read_b128 v[124:127], v103
	v_mfma_f32_32x32x16_f16 v[34:49], v[132:135], v[148:151], v[34:49]
	ds_read_b128 v[112:115], v101
	v_mfma_f32_32x32x16_f16 v[66:81], v[136:139], v[144:147], v[66:81]
	ds_read_b128 v[128:131], v103 offset:2048
	v_mfma_f32_32x32x16_f16 v[18:33], v[136:139], v[148:151], v[18:33]
	ds_read_b128 v[116:119], v101 offset:2048
	v_mfma_f32_32x32x16_f16 v[50:65], v[140:143], v[144:147], v[50:65]
	ds_read_b128 v[120:123], v101 offset:4096
	v_mfma_f32_32x32x16_f16 v[2:17], v[140:143], v[148:151], v[2:17]
	s_waitcnt lgkmcnt(0)
	v_mfma_f32_32x32x16_f16 v[82:97], v[112:115], v[124:127], v[82:97]
	ds_read_b128 v[144:147], v104
	v_mfma_f32_32x32x16_f16 v[34:49], v[112:115], v[128:131], v[34:49]
	ds_read_b128 v[132:135], v102
	v_mfma_f32_32x32x16_f16 v[66:81], v[116:119], v[124:127], v[66:81]
	ds_read_b128 v[148:151], v104 offset:2048
	v_mfma_f32_32x32x16_f16 v[18:33], v[116:119], v[128:131], v[18:33]
	ds_read_b128 v[136:139], v102 offset:2048
	v_mfma_f32_32x32x16_f16 v[50:65], v[120:123], v[124:127], v[50:65]
	ds_read_b128 v[140:143], v102 offset:4096
	v_mfma_f32_32x32x16_f16 v[2:17], v[120:123], v[128:131], v[2:17]
	s_waitcnt lgkmcnt(0)
	s_barrier
	v_mfma_f32_32x32x16_f16 v[82:97], v[132:135], v[144:147], v[82:97]
	ds_read_b128 v[124:127], v103 offset:28672
	v_mfma_f32_32x32x16_f16 v[34:49], v[132:135], v[148:151], v[34:49]
	ds_read_b128 v[112:115], v101 offset:28672
	v_mfma_f32_32x32x16_f16 v[66:81], v[136:139], v[144:147], v[66:81]
	ds_read_b128 v[128:131], v103 offset:30720
	v_mfma_f32_32x32x16_f16 v[18:33], v[136:139], v[148:151], v[18:33]
	ds_read_b128 v[116:119], v101 offset:30720
	v_mfma_f32_32x32x16_f16 v[50:65], v[140:143], v[144:147], v[50:65]
	ds_read_b128 v[120:123], v101 offset:32768
	v_mfma_f32_32x32x16_f16 v[2:17], v[140:143], v[148:151], v[2:17]
	s_waitcnt lgkmcnt(0)
	v_mfma_f32_32x32x16_f16 v[82:97], v[112:115], v[124:127], v[82:97]
	ds_read_b128 v[144:147], v104 offset:28672
	v_mfma_f32_32x32x16_f16 v[34:49], v[112:115], v[128:131], v[34:49]
	ds_read_b128 v[132:135], v102 offset:28672
	v_mfma_f32_32x32x16_f16 v[66:81], v[116:119], v[124:127], v[66:81]
	ds_read_b128 v[148:151], v104 offset:30720
	v_mfma_f32_32x32x16_f16 v[18:33], v[116:119], v[128:131], v[18:33]
	ds_read_b128 v[136:139], v102 offset:30720
	v_mfma_f32_32x32x16_f16 v[50:65], v[120:123], v[124:127], v[50:65]
	ds_read_b128 v[140:143], v102 offset:32768
	v_mfma_f32_32x32x16_f16 v[2:17], v[120:123], v[128:131], v[2:17]
	s_waitcnt lgkmcnt(0)
	s_barrier
	v_mfma_f32_32x32x16_f16 v[82:97], v[132:135], v[144:147], v[82:97]
	ds_read_b128 v[124:127], v107
	v_mfma_f32_32x32x16_f16 v[34:49], v[132:135], v[148:151], v[34:49]
	ds_read_b128 v[112:115], v105
	v_mfma_f32_32x32x16_f16 v[66:81], v[136:139], v[144:147], v[66:81]
	ds_read_b128 v[128:131], v107 offset:2048
	v_mfma_f32_32x32x16_f16 v[18:33], v[136:139], v[148:151], v[18:33]
	ds_read_b128 v[116:119], v105 offset:2048
	v_mfma_f32_32x32x16_f16 v[50:65], v[140:143], v[144:147], v[50:65]
	ds_read_b128 v[120:123], v105 offset:4096
	v_mfma_f32_32x32x16_f16 v[2:17], v[140:143], v[148:151], v[2:17]
	s_waitcnt lgkmcnt(0)
	v_mfma_f32_32x32x16_f16 v[82:97], v[112:115], v[124:127], v[82:97]
	ds_read_b128 v[144:147], v108
	v_mfma_f32_32x32x16_f16 v[34:49], v[112:115], v[128:131], v[34:49]
	ds_read_b128 v[132:135], v106
	v_mfma_f32_32x32x16_f16 v[66:81], v[116:119], v[124:127], v[66:81]
	ds_read_b128 v[148:151], v108 offset:2048
	v_mfma_f32_32x32x16_f16 v[18:33], v[116:119], v[128:131], v[18:33]
	ds_read_b128 v[136:139], v106 offset:2048
	v_mfma_f32_32x32x16_f16 v[50:65], v[120:123], v[124:127], v[50:65]
	ds_read_b128 v[140:143], v106 offset:4096
	v_mfma_f32_32x32x16_f16 v[2:17], v[120:123], v[128:131], v[2:17]
	s_waitcnt lgkmcnt(0)
	s_barrier
	v_mfma_f32_32x32x16_f16 v[82:97], v[132:135], v[144:147], v[82:97]
	ds_read_b128 v[124:127], v107 offset:28672
	v_mfma_f32_32x32x16_f16 v[34:49], v[132:135], v[148:151], v[34:49]
	ds_read_b128 v[112:115], v105 offset:28672
	v_mfma_f32_32x32x16_f16 v[66:81], v[136:139], v[144:147], v[66:81]
	ds_read_b128 v[128:131], v107 offset:30720
	v_mfma_f32_32x32x16_f16 v[18:33], v[136:139], v[148:151], v[18:33]
	ds_read_b128 v[116:119], v105 offset:30720
	v_mfma_f32_32x32x16_f16 v[50:65], v[140:143], v[144:147], v[50:65]
	ds_read_b128 v[120:123], v105 offset:32768
	v_mfma_f32_32x32x16_f16 v[2:17], v[140:143], v[148:151], v[2:17]
	s_waitcnt lgkmcnt(0)
	v_mfma_f32_32x32x16_f16 v[82:97], v[112:115], v[124:127], v[82:97]
	ds_read_b128 v[144:147], v108 offset:28672
	v_mfma_f32_32x32x16_f16 v[34:49], v[112:115], v[128:131], v[34:49]
	ds_read_b128 v[132:135], v106 offset:28672
	v_mfma_f32_32x32x16_f16 v[66:81], v[116:119], v[124:127], v[66:81]
	ds_read_b128 v[148:151], v108 offset:30720
	v_mfma_f32_32x32x16_f16 v[18:33], v[116:119], v[128:131], v[18:33]
	ds_read_b128 v[136:139], v106 offset:30720
	v_mfma_f32_32x32x16_f16 v[50:65], v[120:123], v[124:127], v[50:65]
	ds_read_b128 v[140:143], v106 offset:32768
	v_mfma_f32_32x32x16_f16 v[2:17], v[120:123], v[128:131], v[2:17]
	s_waitcnt lgkmcnt(0)
	v_mfma_f32_32x32x16_f16 v[82:97], v[132:135], v[144:147], v[82:97]
	v_mfma_f32_32x32x16_f16 v[34:49], v[132:135], v[148:151], v[34:49]
	v_mfma_f32_32x32x16_f16 v[66:81], v[136:139], v[144:147], v[66:81]
	v_mfma_f32_32x32x16_f16 v[18:33], v[136:139], v[148:151], v[18:33]
	v_mfma_f32_32x32x16_f16 v[50:65], v[140:143], v[144:147], v[50:65]
	v_mfma_f32_32x32x16_f16 v[2:17], v[140:143], v[148:151], v[2:17]
	s_branch .LBB1_35
.Lqkv_cv:
	s_barrier
	ds_read_b128 v[124:127], v103
	ds_read_b128 v[112:115], v101
	ds_read_b128 v[128:131], v103 offset:2048
	ds_read_b128 v[116:119], v101 offset:2048
	ds_read_b128 v[120:123], v101 offset:4096
	s_waitcnt lgkmcnt(0)
	v_mfma_f32_32x32x16_f16 v[82:97], v[124:127], v[112:115], v[82:97]
	ds_read_b128 v[144:147], v104
	v_mfma_f32_32x32x16_f16 v[34:49], v[128:131], v[112:115], v[34:49]
	ds_read_b128 v[132:135], v102
	v_mfma_f32_32x32x16_f16 v[66:81], v[124:127], v[116:119], v[66:81]
	ds_read_b128 v[148:151], v104 offset:2048
	v_mfma_f32_32x32x16_f16 v[18:33], v[128:131], v[116:119], v[18:33]
	ds_read_b128 v[136:139], v102 offset:2048
	v_mfma_f32_32x32x16_f16 v[50:65], v[124:127], v[120:123], v[50:65]
	ds_read_b128 v[140:143], v102 offset:4096
	v_mfma_f32_32x32x16_f16 v[2:17], v[128:131], v[120:123], v[2:17]
	s_waitcnt lgkmcnt(0)
	s_barrier
	v_mfma_f32_32x32x16_f16 v[82:97], v[144:147], v[132:135], v[82:97]
	ds_read_b128 v[124:127], v103 offset:28672
	v_mfma_f32_32x32x16_f16 v[34:49], v[148:151], v[132:135], v[34:49]
	ds_read_b128 v[112:115], v101 offset:28672
	v_mfma_f32_32x32x16_f16 v[66:81], v[144:147], v[136:139], v[66:81]
	ds_read_b128 v[128:131], v103 offset:30720
	v_mfma_f32_32x32x16_f16 v[18:33], v[148:151], v[136:139], v[18:33]
	ds_read_b128 v[116:119], v101 offset:30720
	v_mfma_f32_32x32x16_f16 v[50:65], v[144:147], v[140:143], v[50:65]
	ds_read_b128 v[120:123], v101 offset:32768
	v_mfma_f32_32x32x16_f16 v[2:17], v[148:151], v[140:143], v[2:17]
	s_waitcnt lgkmcnt(0)
	v_mfma_f32_32x32x16_f16 v[82:97], v[124:127], v[112:115], v[82:97]
	ds_read_b128 v[144:147], v104 offset:28672
	v_mfma_f32_32x32x16_f16 v[34:49], v[128:131], v[112:115], v[34:49]
	ds_read_b128 v[132:135], v102 offset:28672
	v_mfma_f32_32x32x16_f16 v[66:81], v[124:127], v[116:119], v[66:81]
	ds_read_b128 v[148:151], v104 offset:30720
	v_mfma_f32_32x32x16_f16 v[18:33], v[128:131], v[116:119], v[18:33]
	ds_read_b128 v[136:139], v102 offset:30720
	v_mfma_f32_32x32x16_f16 v[50:65], v[124:127], v[120:123], v[50:65]
	ds_read_b128 v[140:143], v102 offset:32768
	v_mfma_f32_32x32x16_f16 v[2:17], v[128:131], v[120:123], v[2:17]
	s_waitcnt lgkmcnt(0)
	s_barrier
	v_mfma_f32_32x32x16_f16 v[82:97], v[144:147], v[132:135], v[82:97]
	ds_read_b128 v[124:127], v107
	v_mfma_f32_32x32x16_f16 v[34:49], v[148:151], v[132:135], v[34:49]
	ds_read_b128 v[112:115], v105
	v_mfma_f32_32x32x16_f16 v[66:81], v[144:147], v[136:139], v[66:81]
	ds_read_b128 v[128:131], v107 offset:2048
	v_mfma_f32_32x32x16_f16 v[18:33], v[148:151], v[136:139], v[18:33]
	ds_read_b128 v[116:119], v105 offset:2048
	v_mfma_f32_32x32x16_f16 v[50:65], v[144:147], v[140:143], v[50:65]
	ds_read_b128 v[120:123], v105 offset:4096
	v_mfma_f32_32x32x16_f16 v[2:17], v[148:151], v[140:143], v[2:17]
	s_waitcnt lgkmcnt(0)
	v_mfma_f32_32x32x16_f16 v[82:97], v[124:127], v[112:115], v[82:97]
	ds_read_b128 v[144:147], v108
	v_mfma_f32_32x32x16_f16 v[34:49], v[128:131], v[112:115], v[34:49]
	ds_read_b128 v[132:135], v106
	v_mfma_f32_32x32x16_f16 v[66:81], v[124:127], v[116:119], v[66:81]
	ds_read_b128 v[148:151], v108 offset:2048
	v_mfma_f32_32x32x16_f16 v[18:33], v[128:131], v[116:119], v[18:33]
	ds_read_b128 v[136:139], v106 offset:2048
	v_mfma_f32_32x32x16_f16 v[50:65], v[124:127], v[120:123], v[50:65]
	ds_read_b128 v[140:143], v106 offset:4096
	v_mfma_f32_32x32x16_f16 v[2:17], v[128:131], v[120:123], v[2:17]
	s_waitcnt lgkmcnt(0)
	s_barrier
	v_mfma_f32_32x32x16_f16 v[82:97], v[144:147], v[132:135], v[82:97]
	ds_read_b128 v[124:127], v107 offset:28672
	v_mfma_f32_32x32x16_f16 v[34:49], v[148:151], v[132:135], v[34:49]
	ds_read_b128 v[112:115], v105 offset:28672
	v_mfma_f32_32x32x16_f16 v[66:81], v[144:147], v[136:139], v[66:81]
	ds_read_b128 v[128:131], v107 offset:30720
	v_mfma_f32_32x32x16_f16 v[18:33], v[148:151], v[136:139], v[18:33]
	ds_read_b128 v[116:119], v105 offset:30720
	v_mfma_f32_32x32x16_f16 v[50:65], v[144:147], v[140:143], v[50:65]
	ds_read_b128 v[120:123], v105 offset:32768
	v_mfma_f32_32x32x16_f16 v[2:17], v[148:151], v[140:143], v[2:17]
	s_waitcnt lgkmcnt(0)
	v_mfma_f32_32x32x16_f16 v[82:97], v[124:127], v[112:115], v[82:97]
	ds_read_b128 v[144:147], v108 offset:28672
	v_mfma_f32_32x32x16_f16 v[34:49], v[128:131], v[112:115], v[34:49]
	ds_read_b128 v[132:135], v106 offset:28672
	v_mfma_f32_32x32x16_f16 v[66:81], v[124:127], v[116:119], v[66:81]
	ds_read_b128 v[148:151], v108 offset:30720
	v_mfma_f32_32x32x16_f16 v[18:33], v[128:131], v[116:119], v[18:33]
	ds_read_b128 v[136:139], v106 offset:30720
	v_mfma_f32_32x32x16_f16 v[50:65], v[124:127], v[120:123], v[50:65]
	ds_read_b128 v[140:143], v106 offset:32768
	v_mfma_f32_32x32x16_f16 v[2:17], v[128:131], v[120:123], v[2:17]
	s_waitcnt lgkmcnt(0)
	s_barrier
	v_mfma_f32_32x32x16_f16 v[82:97], v[144:147], v[132:135], v[82:97]
	ds_read_b128 v[124:127], v103
	v_mfma_f32_32x32x16_f16 v[34:49], v[148:151], v[132:135], v[34:49]
	ds_read_b128 v[112:115], v101
	v_mfma_f32_32x32x16_f16 v[66:81], v[144:147], v[136:139], v[66:81]
	ds_read_b128 v[128:131], v103 offset:2048
	v_mfma_f32_32x32x16_f16 v[18:33], v[148:151], v[136:139], v[18:33]
	ds_read_b128 v[116:119], v101 offset:2048
	v_mfma_f32_32x32x16_f16 v[50:65], v[144:147], v[140:143], v[50:65]
	ds_read_b128 v[120:123], v101 offset:4096
	v_mfma_f32_32x32x16_f16 v[2:17], v[148:151], v[140:143], v[2:17]
	s_waitcnt lgkmcnt(0)
	v_mfma_f32_32x32x16_f16 v[82:97], v[124:127], v[112:115], v[82:97]
	ds_read_b128 v[144:147], v104
	v_mfma_f32_32x32x16_f16 v[34:49], v[128:131], v[112:115], v[34:49]
	ds_read_b128 v[132:135], v102
	v_mfma_f32_32x32x16_f16 v[66:81], v[124:127], v[116:119], v[66:81]
	ds_read_b128 v[148:151], v104 offset:2048
	v_mfma_f32_32x32x16_f16 v[18:33], v[128:131], v[116:119], v[18:33]
	ds_read_b128 v[136:139], v102 offset:2048
	v_mfma_f32_32x32x16_f16 v[50:65], v[124:127], v[120:123], v[50:65]
	ds_read_b128 v[140:143], v102 offset:4096
	v_mfma_f32_32x32x16_f16 v[2:17], v[128:131], v[120:123], v[2:17]
	s_waitcnt lgkmcnt(0)
	s_barrier
	v_mfma_f32_32x32x16_f16 v[82:97], v[144:147], v[132:135], v[82:97]
	ds_read_b128 v[124:127], v103 offset:28672
	v_mfma_f32_32x32x16_f16 v[34:49], v[148:151], v[132:135], v[34:49]
	ds_read_b128 v[112:115], v101 offset:28672
	v_mfma_f32_32x32x16_f16 v[66:81], v[144:147], v[136:139], v[66:81]
	ds_read_b128 v[128:131], v103 offset:30720
	v_mfma_f32_32x32x16_f16 v[18:33], v[148:151], v[136:139], v[18:33]
	ds_read_b128 v[116:119], v101 offset:30720
	v_mfma_f32_32x32x16_f16 v[50:65], v[144:147], v[140:143], v[50:65]
	ds_read_b128 v[120:123], v101 offset:32768
	v_mfma_f32_32x32x16_f16 v[2:17], v[148:151], v[140:143], v[2:17]
	s_waitcnt lgkmcnt(0)
	v_mfma_f32_32x32x16_f16 v[82:97], v[124:127], v[112:115], v[82:97]
	ds_read_b128 v[144:147], v104 offset:28672
	v_mfma_f32_32x32x16_f16 v[34:49], v[128:131], v[112:115], v[34:49]
	ds_read_b128 v[132:135], v102 offset:28672
	v_mfma_f32_32x32x16_f16 v[66:81], v[124:127], v[116:119], v[66:81]
	ds_read_b128 v[148:151], v104 offset:30720
	v_mfma_f32_32x32x16_f16 v[18:33], v[128:131], v[116:119], v[18:33]
	ds_read_b128 v[136:139], v102 offset:30720
	v_mfma_f32_32x32x16_f16 v[50:65], v[124:127], v[120:123], v[50:65]
	ds_read_b128 v[140:143], v102 offset:32768
	v_mfma_f32_32x32x16_f16 v[2:17], v[128:131], v[120:123], v[2:17]
	s_waitcnt lgkmcnt(0)
	s_barrier
	v_mfma_f32_32x32x16_f16 v[82:97], v[144:147], v[132:135], v[82:97]
	ds_read_b128 v[124:127], v107
	v_mfma_f32_32x32x16_f16 v[34:49], v[148:151], v[132:135], v[34:49]
	ds_read_b128 v[112:115], v105
	v_mfma_f32_32x32x16_f16 v[66:81], v[144:147], v[136:139], v[66:81]
	ds_read_b128 v[128:131], v107 offset:2048
	v_mfma_f32_32x32x16_f16 v[18:33], v[148:151], v[136:139], v[18:33]
	ds_read_b128 v[116:119], v105 offset:2048
	v_mfma_f32_32x32x16_f16 v[50:65], v[144:147], v[140:143], v[50:65]
	ds_read_b128 v[120:123], v105 offset:4096
	v_mfma_f32_32x32x16_f16 v[2:17], v[148:151], v[140:143], v[2:17]
	s_waitcnt lgkmcnt(0)
	v_mfma_f32_32x32x16_f16 v[82:97], v[124:127], v[112:115], v[82:97]
	ds_read_b128 v[144:147], v108
	v_mfma_f32_32x32x16_f16 v[34:49], v[128:131], v[112:115], v[34:49]
	ds_read_b128 v[132:135], v106
	v_mfma_f32_32x32x16_f16 v[66:81], v[124:127], v[116:119], v[66:81]
	ds_read_b128 v[148:151], v108 offset:2048
	v_mfma_f32_32x32x16_f16 v[18:33], v[128:131], v[116:119], v[18:33]
	ds_read_b128 v[136:139], v106 offset:2048
	v_mfma_f32_32x32x16_f16 v[50:65], v[124:127], v[120:123], v[50:65]
	ds_read_b128 v[140:143], v106 offset:4096
	v_mfma_f32_32x32x16_f16 v[2:17], v[128:131], v[120:123], v[2:17]
	s_waitcnt lgkmcnt(0)
	s_barrier
	v_mfma_f32_32x32x16_f16 v[82:97], v[144:147], v[132:135], v[82:97]
	ds_read_b128 v[124:127], v107 offset:28672
	v_mfma_f32_32x32x16_f16 v[34:49], v[148:151], v[132:135], v[34:49]
	ds_read_b128 v[112:115], v105 offset:28672
	v_mfma_f32_32x32x16_f16 v[66:81], v[144:147], v[136:139], v[66:81]
	ds_read_b128 v[128:131], v107 offset:30720
	v_mfma_f32_32x32x16_f16 v[18:33], v[148:151], v[136:139], v[18:33]
	ds_read_b128 v[116:119], v105 offset:30720
	v_mfma_f32_32x32x16_f16 v[50:65], v[144:147], v[140:143], v[50:65]
	ds_read_b128 v[120:123], v105 offset:32768
	v_mfma_f32_32x32x16_f16 v[2:17], v[148:151], v[140:143], v[2:17]
	s_waitcnt lgkmcnt(0)
	v_mfma_f32_32x32x16_f16 v[82:97], v[124:127], v[112:115], v[82:97]
	ds_read_b128 v[144:147], v108 offset:28672
	v_mfma_f32_32x32x16_f16 v[34:49], v[128:131], v[112:115], v[34:49]
	ds_read_b128 v[132:135], v106 offset:28672
	v_mfma_f32_32x32x16_f16 v[66:81], v[124:127], v[116:119], v[66:81]
	ds_read_b128 v[148:151], v108 offset:30720
	v_mfma_f32_32x32x16_f16 v[18:33], v[128:131], v[116:119], v[18:33]
	ds_read_b128 v[136:139], v106 offset:30720
	v_mfma_f32_32x32x16_f16 v[50:65], v[124:127], v[120:123], v[50:65]
	ds_read_b128 v[140:143], v106 offset:32768
	v_mfma_f32_32x32x16_f16 v[2:17], v[128:131], v[120:123], v[2:17]
	s_waitcnt lgkmcnt(0)
	s_barrier
	v_mfma_f32_32x32x16_f16 v[82:97], v[144:147], v[132:135], v[82:97]
	ds_read_b128 v[124:127], v103
	v_mfma_f32_32x32x16_f16 v[34:49], v[148:151], v[132:135], v[34:49]
	ds_read_b128 v[112:115], v101
	v_mfma_f32_32x32x16_f16 v[66:81], v[144:147], v[136:139], v[66:81]
	ds_read_b128 v[128:131], v103 offset:2048
	v_mfma_f32_32x32x16_f16 v[18:33], v[148:151], v[136:139], v[18:33]
	ds_read_b128 v[116:119], v101 offset:2048
	v_mfma_f32_32x32x16_f16 v[50:65], v[144:147], v[140:143], v[50:65]
	ds_read_b128 v[120:123], v101 offset:4096
	v_mfma_f32_32x32x16_f16 v[2:17], v[148:151], v[140:143], v[2:17]
	s_waitcnt lgkmcnt(0)
	v_mfma_f32_32x32x16_f16 v[82:97], v[124:127], v[112:115], v[82:97]
	ds_read_b128 v[144:147], v104
	v_mfma_f32_32x32x16_f16 v[34:49], v[128:131], v[112:115], v[34:49]
	ds_read_b128 v[132:135], v102
	v_mfma_f32_32x32x16_f16 v[66:81], v[124:127], v[116:119], v[66:81]
	ds_read_b128 v[148:151], v104 offset:2048
	v_mfma_f32_32x32x16_f16 v[18:33], v[128:131], v[116:119], v[18:33]
	ds_read_b128 v[136:139], v102 offset:2048
	v_mfma_f32_32x32x16_f16 v[50:65], v[124:127], v[120:123], v[50:65]
	ds_read_b128 v[140:143], v102 offset:4096
	v_mfma_f32_32x32x16_f16 v[2:17], v[128:131], v[120:123], v[2:17]
	s_waitcnt lgkmcnt(0)
	s_barrier
	v_mfma_f32_32x32x16_f16 v[82:97], v[144:147], v[132:135], v[82:97]
	ds_read_b128 v[124:127], v103 offset:28672
	v_mfma_f32_32x32x16_f16 v[34:49], v[148:151], v[132:135], v[34:49]
	ds_read_b128 v[112:115], v101 offset:28672
	v_mfma_f32_32x32x16_f16 v[66:81], v[144:147], v[136:139], v[66:81]
	ds_read_b128 v[128:131], v103 offset:30720
	v_mfma_f32_32x32x16_f16 v[18:33], v[148:151], v[136:139], v[18:33]
	ds_read_b128 v[116:119], v101 offset:30720
	v_mfma_f32_32x32x16_f16 v[50:65], v[144:147], v[140:143], v[50:65]
	ds_read_b128 v[120:123], v101 offset:32768
	v_mfma_f32_32x32x16_f16 v[2:17], v[148:151], v[140:143], v[2:17]
	s_waitcnt lgkmcnt(0)
	v_mfma_f32_32x32x16_f16 v[82:97], v[124:127], v[112:115], v[82:97]
	ds_read_b128 v[144:147], v104 offset:28672
	v_mfma_f32_32x32x16_f16 v[34:49], v[128:131], v[112:115], v[34:49]
	ds_read_b128 v[132:135], v102 offset:28672
	v_mfma_f32_32x32x16_f16 v[66:81], v[124:127], v[116:119], v[66:81]
	ds_read_b128 v[148:151], v104 offset:30720
	v_mfma_f32_32x32x16_f16 v[18:33], v[128:131], v[116:119], v[18:33]
	ds_read_b128 v[136:139], v102 offset:30720
	v_mfma_f32_32x32x16_f16 v[50:65], v[124:127], v[120:123], v[50:65]
	ds_read_b128 v[140:143], v102 offset:32768
	v_mfma_f32_32x32x16_f16 v[2:17], v[128:131], v[120:123], v[2:17]
	s_waitcnt lgkmcnt(0)
	s_barrier
	v_mfma_f32_32x32x16_f16 v[82:97], v[144:147], v[132:135], v[82:97]
	ds_read_b128 v[124:127], v107
	v_mfma_f32_32x32x16_f16 v[34:49], v[148:151], v[132:135], v[34:49]
	ds_read_b128 v[112:115], v105
	v_mfma_f32_32x32x16_f16 v[66:81], v[144:147], v[136:139], v[66:81]
	ds_read_b128 v[128:131], v107 offset:2048
	v_mfma_f32_32x32x16_f16 v[18:33], v[148:151], v[136:139], v[18:33]
	ds_read_b128 v[116:119], v105 offset:2048
	v_mfma_f32_32x32x16_f16 v[50:65], v[144:147], v[140:143], v[50:65]
	ds_read_b128 v[120:123], v105 offset:4096
	v_mfma_f32_32x32x16_f16 v[2:17], v[148:151], v[140:143], v[2:17]
	s_waitcnt lgkmcnt(0)
	v_mfma_f32_32x32x16_f16 v[82:97], v[124:127], v[112:115], v[82:97]
	ds_read_b128 v[144:147], v108
	v_mfma_f32_32x32x16_f16 v[34:49], v[128:131], v[112:115], v[34:49]
	ds_read_b128 v[132:135], v106
	v_mfma_f32_32x32x16_f16 v[66:81], v[124:127], v[116:119], v[66:81]
	ds_read_b128 v[148:151], v108 offset:2048
	v_mfma_f32_32x32x16_f16 v[18:33], v[128:131], v[116:119], v[18:33]
	ds_read_b128 v[136:139], v106 offset:2048
	v_mfma_f32_32x32x16_f16 v[50:65], v[124:127], v[120:123], v[50:65]
	ds_read_b128 v[140:143], v106 offset:4096
	v_mfma_f32_32x32x16_f16 v[2:17], v[128:131], v[120:123], v[2:17]
	s_waitcnt lgkmcnt(0)
	s_barrier
	v_mfma_f32_32x32x16_f16 v[82:97], v[144:147], v[132:135], v[82:97]
	ds_read_b128 v[124:127], v107 offset:28672
	v_mfma_f32_32x32x16_f16 v[34:49], v[148:151], v[132:135], v[34:49]
	ds_read_b128 v[112:115], v105 offset:28672
	v_mfma_f32_32x32x16_f16 v[66:81], v[144:147], v[136:139], v[66:81]
	ds_read_b128 v[128:131], v107 offset:30720
	v_mfma_f32_32x32x16_f16 v[18:33], v[148:151], v[136:139], v[18:33]
	ds_read_b128 v[116:119], v105 offset:30720
	v_mfma_f32_32x32x16_f16 v[50:65], v[144:147], v[140:143], v[50:65]
	ds_read_b128 v[120:123], v105 offset:32768
	v_mfma_f32_32x32x16_f16 v[2:17], v[148:151], v[140:143], v[2:17]
	s_waitcnt lgkmcnt(0)
	v_mfma_f32_32x32x16_f16 v[82:97], v[124:127], v[112:115], v[82:97]
	ds_read_b128 v[144:147], v108 offset:28672
	v_mfma_f32_32x32x16_f16 v[34:49], v[128:131], v[112:115], v[34:49]
	ds_read_b128 v[132:135], v106 offset:28672
	v_mfma_f32_32x32x16_f16 v[66:81], v[124:127], v[116:119], v[66:81]
	ds_read_b128 v[148:151], v108 offset:30720
	v_mfma_f32_32x32x16_f16 v[18:33], v[128:131], v[116:119], v[18:33]
	ds_read_b128 v[136:139], v106 offset:30720
	v_mfma_f32_32x32x16_f16 v[50:65], v[124:127], v[120:123], v[50:65]
	ds_read_b128 v[140:143], v106 offset:32768
	v_mfma_f32_32x32x16_f16 v[2:17], v[128:131], v[120:123], v[2:17]
	s_waitcnt lgkmcnt(0)
	s_barrier
	v_mfma_f32_32x32x16_f16 v[82:97], v[144:147], v[132:135], v[82:97]
	ds_read_b128 v[124:127], v103
	v_mfma_f32_32x32x16_f16 v[34:49], v[148:151], v[132:135], v[34:49]
	ds_read_b128 v[112:115], v101
	v_mfma_f32_32x32x16_f16 v[66:81], v[144:147], v[136:139], v[66:81]
	ds_read_b128 v[128:131], v103 offset:2048
	v_mfma_f32_32x32x16_f16 v[18:33], v[148:151], v[136:139], v[18:33]
	ds_read_b128 v[116:119], v101 offset:2048
	v_mfma_f32_32x32x16_f16 v[50:65], v[144:147], v[140:143], v[50:65]
	ds_read_b128 v[120:123], v101 offset:4096
	v_mfma_f32_32x32x16_f16 v[2:17], v[148:151], v[140:143], v[2:17]
	s_waitcnt lgkmcnt(0)
	v_mfma_f32_32x32x16_f16 v[82:97], v[124:127], v[112:115], v[82:97]
	ds_read_b128 v[144:147], v104
	v_mfma_f32_32x32x16_f16 v[34:49], v[128:131], v[112:115], v[34:49]
	ds_read_b128 v[132:135], v102
	v_mfma_f32_32x32x16_f16 v[66:81], v[124:127], v[116:119], v[66:81]
	ds_read_b128 v[148:151], v104 offset:2048
	v_mfma_f32_32x32x16_f16 v[18:33], v[128:131], v[116:119], v[18:33]
	ds_read_b128 v[136:139], v102 offset:2048
	v_mfma_f32_32x32x16_f16 v[50:65], v[124:127], v[120:123], v[50:65]
	ds_read_b128 v[140:143], v102 offset:4096
	v_mfma_f32_32x32x16_f16 v[2:17], v[128:131], v[120:123], v[2:17]
	s_waitcnt lgkmcnt(0)
	s_barrier
	v_mfma_f32_32x32x16_f16 v[82:97], v[144:147], v[132:135], v[82:97]
	ds_read_b128 v[124:127], v103 offset:28672
	v_mfma_f32_32x32x16_f16 v[34:49], v[148:151], v[132:135], v[34:49]
	ds_read_b128 v[112:115], v101 offset:28672
	v_mfma_f32_32x32x16_f16 v[66:81], v[144:147], v[136:139], v[66:81]
	ds_read_b128 v[128:131], v103 offset:30720
	v_mfma_f32_32x32x16_f16 v[18:33], v[148:151], v[136:139], v[18:33]
	ds_read_b128 v[116:119], v101 offset:30720
	v_mfma_f32_32x32x16_f16 v[50:65], v[144:147], v[140:143], v[50:65]
	ds_read_b128 v[120:123], v101 offset:32768
	v_mfma_f32_32x32x16_f16 v[2:17], v[148:151], v[140:143], v[2:17]
	s_waitcnt lgkmcnt(0)
	v_mfma_f32_32x32x16_f16 v[82:97], v[124:127], v[112:115], v[82:97]
	ds_read_b128 v[144:147], v104 offset:28672
	v_mfma_f32_32x32x16_f16 v[34:49], v[128:131], v[112:115], v[34:49]
	ds_read_b128 v[132:135], v102 offset:28672
	v_mfma_f32_32x32x16_f16 v[66:81], v[124:127], v[116:119], v[66:81]
	ds_read_b128 v[148:151], v104 offset:30720
	v_mfma_f32_32x32x16_f16 v[18:33], v[128:131], v[116:119], v[18:33]
	ds_read_b128 v[136:139], v102 offset:30720
	v_mfma_f32_32x32x16_f16 v[50:65], v[124:127], v[120:123], v[50:65]
	ds_read_b128 v[140:143], v102 offset:32768
	v_mfma_f32_32x32x16_f16 v[2:17], v[128:131], v[120:123], v[2:17]
	s_waitcnt lgkmcnt(0)
	s_barrier
	v_mfma_f32_32x32x16_f16 v[82:97], v[144:147], v[132:135], v[82:97]
	ds_read_b128 v[124:127], v107
	v_mfma_f32_32x32x16_f16 v[34:49], v[148:151], v[132:135], v[34:49]
	ds_read_b128 v[112:115], v105
	v_mfma_f32_32x32x16_f16 v[66:81], v[144:147], v[136:139], v[66:81]
	ds_read_b128 v[128:131], v107 offset:2048
	v_mfma_f32_32x32x16_f16 v[18:33], v[148:151], v[136:139], v[18:33]
	ds_read_b128 v[116:119], v105 offset:2048
	v_mfma_f32_32x32x16_f16 v[50:65], v[144:147], v[140:143], v[50:65]
	ds_read_b128 v[120:123], v105 offset:4096
	v_mfma_f32_32x32x16_f16 v[2:17], v[148:151], v[140:143], v[2:17]
	s_waitcnt lgkmcnt(0)
	v_mfma_f32_32x32x16_f16 v[82:97], v[124:127], v[112:115], v[82:97]
	ds_read_b128 v[144:147], v108
	v_mfma_f32_32x32x16_f16 v[34:49], v[128:131], v[112:115], v[34:49]
	ds_read_b128 v[132:135], v106
	v_mfma_f32_32x32x16_f16 v[66:81], v[124:127], v[116:119], v[66:81]
	ds_read_b128 v[148:151], v108 offset:2048
	v_mfma_f32_32x32x16_f16 v[18:33], v[128:131], v[116:119], v[18:33]
	ds_read_b128 v[136:139], v106 offset:2048
	v_mfma_f32_32x32x16_f16 v[50:65], v[124:127], v[120:123], v[50:65]
	ds_read_b128 v[140:143], v106 offset:4096
	v_mfma_f32_32x32x16_f16 v[2:17], v[128:131], v[120:123], v[2:17]
	s_waitcnt lgkmcnt(0)
	s_barrier
	v_mfma_f32_32x32x16_f16 v[82:97], v[144:147], v[132:135], v[82:97]
	ds_read_b128 v[124:127], v107 offset:28672
	v_mfma_f32_32x32x16_f16 v[34:49], v[148:151], v[132:135], v[34:49]
	ds_read_b128 v[112:115], v105 offset:28672
	v_mfma_f32_32x32x16_f16 v[66:81], v[144:147], v[136:139], v[66:81]
	ds_read_b128 v[128:131], v107 offset:30720
	v_mfma_f32_32x32x16_f16 v[18:33], v[148:151], v[136:139], v[18:33]
	ds_read_b128 v[116:119], v105 offset:30720
	v_mfma_f32_32x32x16_f16 v[50:65], v[144:147], v[140:143], v[50:65]
	ds_read_b128 v[120:123], v105 offset:32768
	v_mfma_f32_32x32x16_f16 v[2:17], v[148:151], v[140:143], v[2:17]
	s_waitcnt lgkmcnt(0)
	v_mfma_f32_32x32x16_f16 v[82:97], v[124:127], v[112:115], v[82:97]
	ds_read_b128 v[144:147], v108 offset:28672
	v_mfma_f32_32x32x16_f16 v[34:49], v[128:131], v[112:115], v[34:49]
	ds_read_b128 v[132:135], v106 offset:28672
	v_mfma_f32_32x32x16_f16 v[66:81], v[124:127], v[116:119], v[66:81]
	ds_read_b128 v[148:151], v108 offset:30720
	v_mfma_f32_32x32x16_f16 v[18:33], v[128:131], v[116:119], v[18:33]
	ds_read_b128 v[136:139], v106 offset:30720
	v_mfma_f32_32x32x16_f16 v[50:65], v[124:127], v[120:123], v[50:65]
	ds_read_b128 v[140:143], v106 offset:32768
	v_mfma_f32_32x32x16_f16 v[2:17], v[128:131], v[120:123], v[2:17]
	s_waitcnt lgkmcnt(0)
	s_barrier
	v_mfma_f32_32x32x16_f16 v[82:97], v[144:147], v[132:135], v[82:97]
	ds_read_b128 v[124:127], v103
	v_mfma_f32_32x32x16_f16 v[34:49], v[148:151], v[132:135], v[34:49]
	ds_read_b128 v[112:115], v101
	v_mfma_f32_32x32x16_f16 v[66:81], v[144:147], v[136:139], v[66:81]
	ds_read_b128 v[128:131], v103 offset:2048
	v_mfma_f32_32x32x16_f16 v[18:33], v[148:151], v[136:139], v[18:33]
	ds_read_b128 v[116:119], v101 offset:2048
	v_mfma_f32_32x32x16_f16 v[50:65], v[144:147], v[140:143], v[50:65]
	ds_read_b128 v[120:123], v101 offset:4096
	v_mfma_f32_32x32x16_f16 v[2:17], v[148:151], v[140:143], v[2:17]
	s_waitcnt lgkmcnt(0)
	v_mfma_f32_32x32x16_f16 v[82:97], v[124:127], v[112:115], v[82:97]
	ds_read_b128 v[144:147], v104
	v_mfma_f32_32x32x16_f16 v[34:49], v[128:131], v[112:115], v[34:49]
	ds_read_b128 v[132:135], v102
	v_mfma_f32_32x32x16_f16 v[66:81], v[124:127], v[116:119], v[66:81]
	ds_read_b128 v[148:151], v104 offset:2048
	v_mfma_f32_32x32x16_f16 v[18:33], v[128:131], v[116:119], v[18:33]
	ds_read_b128 v[136:139], v102 offset:2048
	v_mfma_f32_32x32x16_f16 v[50:65], v[124:127], v[120:123], v[50:65]
	ds_read_b128 v[140:143], v102 offset:4096
	v_mfma_f32_32x32x16_f16 v[2:17], v[128:131], v[120:123], v[2:17]
	s_waitcnt lgkmcnt(0)
	s_barrier
	v_mfma_f32_32x32x16_f16 v[82:97], v[144:147], v[132:135], v[82:97]
	ds_read_b128 v[124:127], v103 offset:28672
	v_mfma_f32_32x32x16_f16 v[34:49], v[148:151], v[132:135], v[34:49]
	ds_read_b128 v[112:115], v101 offset:28672
	v_mfma_f32_32x32x16_f16 v[66:81], v[144:147], v[136:139], v[66:81]
	ds_read_b128 v[128:131], v103 offset:30720
	v_mfma_f32_32x32x16_f16 v[18:33], v[148:151], v[136:139], v[18:33]
	ds_read_b128 v[116:119], v101 offset:30720
	v_mfma_f32_32x32x16_f16 v[50:65], v[144:147], v[140:143], v[50:65]
	ds_read_b128 v[120:123], v101 offset:32768
	v_mfma_f32_32x32x16_f16 v[2:17], v[148:151], v[140:143], v[2:17]
	s_waitcnt lgkmcnt(0)
	v_mfma_f32_32x32x16_f16 v[82:97], v[124:127], v[112:115], v[82:97]
	ds_read_b128 v[144:147], v104 offset:28672
	v_mfma_f32_32x32x16_f16 v[34:49], v[128:131], v[112:115], v[34:49]
	ds_read_b128 v[132:135], v102 offset:28672
	v_mfma_f32_32x32x16_f16 v[66:81], v[124:127], v[116:119], v[66:81]
	ds_read_b128 v[148:151], v104 offset:30720
	v_mfma_f32_32x32x16_f16 v[18:33], v[128:131], v[116:119], v[18:33]
	ds_read_b128 v[136:139], v102 offset:30720
	v_mfma_f32_32x32x16_f16 v[50:65], v[124:127], v[120:123], v[50:65]
	ds_read_b128 v[140:143], v102 offset:32768
	v_mfma_f32_32x32x16_f16 v[2:17], v[128:131], v[120:123], v[2:17]
	s_waitcnt lgkmcnt(0)
	s_barrier
	v_mfma_f32_32x32x16_f16 v[82:97], v[144:147], v[132:135], v[82:97]
	ds_read_b128 v[124:127], v107
	v_mfma_f32_32x32x16_f16 v[34:49], v[148:151], v[132:135], v[34:49]
	ds_read_b128 v[112:115], v105
	v_mfma_f32_32x32x16_f16 v[66:81], v[144:147], v[136:139], v[66:81]
	ds_read_b128 v[128:131], v107 offset:2048
	v_mfma_f32_32x32x16_f16 v[18:33], v[148:151], v[136:139], v[18:33]
	ds_read_b128 v[116:119], v105 offset:2048
	v_mfma_f32_32x32x16_f16 v[50:65], v[144:147], v[140:143], v[50:65]
	ds_read_b128 v[120:123], v105 offset:4096
	v_mfma_f32_32x32x16_f16 v[2:17], v[148:151], v[140:143], v[2:17]
	s_waitcnt lgkmcnt(0)
	v_mfma_f32_32x32x16_f16 v[82:97], v[124:127], v[112:115], v[82:97]
	ds_read_b128 v[144:147], v108
	v_mfma_f32_32x32x16_f16 v[34:49], v[128:131], v[112:115], v[34:49]
	ds_read_b128 v[132:135], v106
	v_mfma_f32_32x32x16_f16 v[66:81], v[124:127], v[116:119], v[66:81]
	ds_read_b128 v[148:151], v108 offset:2048
	v_mfma_f32_32x32x16_f16 v[18:33], v[128:131], v[116:119], v[18:33]
	ds_read_b128 v[136:139], v106 offset:2048
	v_mfma_f32_32x32x16_f16 v[50:65], v[124:127], v[120:123], v[50:65]
	ds_read_b128 v[140:143], v106 offset:4096
	v_mfma_f32_32x32x16_f16 v[2:17], v[128:131], v[120:123], v[2:17]
	s_waitcnt lgkmcnt(0)
	s_barrier
	v_mfma_f32_32x32x16_f16 v[82:97], v[144:147], v[132:135], v[82:97]
	ds_read_b128 v[124:127], v107 offset:28672
	v_mfma_f32_32x32x16_f16 v[34:49], v[148:151], v[132:135], v[34:49]
	ds_read_b128 v[112:115], v105 offset:28672
	v_mfma_f32_32x32x16_f16 v[66:81], v[144:147], v[136:139], v[66:81]
	ds_read_b128 v[128:131], v107 offset:30720
	v_mfma_f32_32x32x16_f16 v[18:33], v[148:151], v[136:139], v[18:33]
	ds_read_b128 v[116:119], v105 offset:30720
	v_mfma_f32_32x32x16_f16 v[50:65], v[144:147], v[140:143], v[50:65]
	ds_read_b128 v[120:123], v105 offset:32768
	v_mfma_f32_32x32x16_f16 v[2:17], v[148:151], v[140:143], v[2:17]
	s_waitcnt lgkmcnt(0)
	v_mfma_f32_32x32x16_f16 v[82:97], v[124:127], v[112:115], v[82:97]
	ds_read_b128 v[144:147], v108 offset:28672
	v_mfma_f32_32x32x16_f16 v[34:49], v[128:131], v[112:115], v[34:49]
	ds_read_b128 v[132:135], v106 offset:28672
	v_mfma_f32_32x32x16_f16 v[66:81], v[124:127], v[116:119], v[66:81]
	ds_read_b128 v[148:151], v108 offset:30720
	v_mfma_f32_32x32x16_f16 v[18:33], v[128:131], v[116:119], v[18:33]
	ds_read_b128 v[136:139], v106 offset:30720
	v_mfma_f32_32x32x16_f16 v[50:65], v[124:127], v[120:123], v[50:65]
	ds_read_b128 v[140:143], v106 offset:32768
	v_mfma_f32_32x32x16_f16 v[2:17], v[128:131], v[120:123], v[2:17]
	s_waitcnt lgkmcnt(0)
	s_barrier
	v_mfma_f32_32x32x16_f16 v[82:97], v[144:147], v[132:135], v[82:97]
	ds_read_b128 v[124:127], v103
	v_mfma_f32_32x32x16_f16 v[34:49], v[148:151], v[132:135], v[34:49]
	ds_read_b128 v[112:115], v101
	v_mfma_f32_32x32x16_f16 v[66:81], v[144:147], v[136:139], v[66:81]
	ds_read_b128 v[128:131], v103 offset:2048
	v_mfma_f32_32x32x16_f16 v[18:33], v[148:151], v[136:139], v[18:33]
	ds_read_b128 v[116:119], v101 offset:2048
	v_mfma_f32_32x32x16_f16 v[50:65], v[144:147], v[140:143], v[50:65]
	ds_read_b128 v[120:123], v101 offset:4096
	v_mfma_f32_32x32x16_f16 v[2:17], v[148:151], v[140:143], v[2:17]
	s_waitcnt lgkmcnt(0)
	v_mfma_f32_32x32x16_f16 v[82:97], v[124:127], v[112:115], v[82:97]
	ds_read_b128 v[144:147], v104
	v_mfma_f32_32x32x16_f16 v[34:49], v[128:131], v[112:115], v[34:49]
	ds_read_b128 v[132:135], v102
	v_mfma_f32_32x32x16_f16 v[66:81], v[124:127], v[116:119], v[66:81]
	ds_read_b128 v[148:151], v104 offset:2048
	v_mfma_f32_32x32x16_f16 v[18:33], v[128:131], v[116:119], v[18:33]
	ds_read_b128 v[136:139], v102 offset:2048
	v_mfma_f32_32x32x16_f16 v[50:65], v[124:127], v[120:123], v[50:65]
	ds_read_b128 v[140:143], v102 offset:4096
	v_mfma_f32_32x32x16_f16 v[2:17], v[128:131], v[120:123], v[2:17]
	s_waitcnt lgkmcnt(0)
	s_barrier
	v_mfma_f32_32x32x16_f16 v[82:97], v[144:147], v[132:135], v[82:97]
	ds_read_b128 v[124:127], v103 offset:28672
	v_mfma_f32_32x32x16_f16 v[34:49], v[148:151], v[132:135], v[34:49]
	ds_read_b128 v[112:115], v101 offset:28672
	v_mfma_f32_32x32x16_f16 v[66:81], v[144:147], v[136:139], v[66:81]
	ds_read_b128 v[128:131], v103 offset:30720
	v_mfma_f32_32x32x16_f16 v[18:33], v[148:151], v[136:139], v[18:33]
	ds_read_b128 v[116:119], v101 offset:30720
	v_mfma_f32_32x32x16_f16 v[50:65], v[144:147], v[140:143], v[50:65]
	ds_read_b128 v[120:123], v101 offset:32768
	v_mfma_f32_32x32x16_f16 v[2:17], v[148:151], v[140:143], v[2:17]
	s_waitcnt lgkmcnt(0)
	v_mfma_f32_32x32x16_f16 v[82:97], v[124:127], v[112:115], v[82:97]
	ds_read_b128 v[144:147], v104 offset:28672
	v_mfma_f32_32x32x16_f16 v[34:49], v[128:131], v[112:115], v[34:49]
	ds_read_b128 v[132:135], v102 offset:28672
	v_mfma_f32_32x32x16_f16 v[66:81], v[124:127], v[116:119], v[66:81]
	ds_read_b128 v[148:151], v104 offset:30720
	v_mfma_f32_32x32x16_f16 v[18:33], v[128:131], v[116:119], v[18:33]
	ds_read_b128 v[136:139], v102 offset:30720
	v_mfma_f32_32x32x16_f16 v[50:65], v[124:127], v[120:123], v[50:65]
	ds_read_b128 v[140:143], v102 offset:32768
	v_mfma_f32_32x32x16_f16 v[2:17], v[128:131], v[120:123], v[2:17]
	s_waitcnt lgkmcnt(0)
	s_barrier
	v_mfma_f32_32x32x16_f16 v[82:97], v[144:147], v[132:135], v[82:97]
	ds_read_b128 v[124:127], v107
	v_mfma_f32_32x32x16_f16 v[34:49], v[148:151], v[132:135], v[34:49]
	ds_read_b128 v[112:115], v105
	v_mfma_f32_32x32x16_f16 v[66:81], v[144:147], v[136:139], v[66:81]
	ds_read_b128 v[128:131], v107 offset:2048
	v_mfma_f32_32x32x16_f16 v[18:33], v[148:151], v[136:139], v[18:33]
	ds_read_b128 v[116:119], v105 offset:2048
	v_mfma_f32_32x32x16_f16 v[50:65], v[144:147], v[140:143], v[50:65]
	ds_read_b128 v[120:123], v105 offset:4096
	v_mfma_f32_32x32x16_f16 v[2:17], v[148:151], v[140:143], v[2:17]
	s_waitcnt lgkmcnt(0)
	v_mfma_f32_32x32x16_f16 v[82:97], v[124:127], v[112:115], v[82:97]
	ds_read_b128 v[144:147], v108
	v_mfma_f32_32x32x16_f16 v[34:49], v[128:131], v[112:115], v[34:49]
	ds_read_b128 v[132:135], v106
	v_mfma_f32_32x32x16_f16 v[66:81], v[124:127], v[116:119], v[66:81]
	ds_read_b128 v[148:151], v108 offset:2048
	v_mfma_f32_32x32x16_f16 v[18:33], v[128:131], v[116:119], v[18:33]
	ds_read_b128 v[136:139], v106 offset:2048
	v_mfma_f32_32x32x16_f16 v[50:65], v[124:127], v[120:123], v[50:65]
	ds_read_b128 v[140:143], v106 offset:4096
	v_mfma_f32_32x32x16_f16 v[2:17], v[128:131], v[120:123], v[2:17]
	s_waitcnt lgkmcnt(0)
	s_barrier
	v_mfma_f32_32x32x16_f16 v[82:97], v[144:147], v[132:135], v[82:97]
	ds_read_b128 v[124:127], v107 offset:28672
	v_mfma_f32_32x32x16_f16 v[34:49], v[148:151], v[132:135], v[34:49]
	ds_read_b128 v[112:115], v105 offset:28672
	v_mfma_f32_32x32x16_f16 v[66:81], v[144:147], v[136:139], v[66:81]
	ds_read_b128 v[128:131], v107 offset:30720
	v_mfma_f32_32x32x16_f16 v[18:33], v[148:151], v[136:139], v[18:33]
	ds_read_b128 v[116:119], v105 offset:30720
	v_mfma_f32_32x32x16_f16 v[50:65], v[144:147], v[140:143], v[50:65]
	ds_read_b128 v[120:123], v105 offset:32768
	v_mfma_f32_32x32x16_f16 v[2:17], v[148:151], v[140:143], v[2:17]
	s_waitcnt lgkmcnt(0)
	v_mfma_f32_32x32x16_f16 v[82:97], v[124:127], v[112:115], v[82:97]
	ds_read_b128 v[144:147], v108 offset:28672
	v_mfma_f32_32x32x16_f16 v[34:49], v[128:131], v[112:115], v[34:49]
	ds_read_b128 v[132:135], v106 offset:28672
	v_mfma_f32_32x32x16_f16 v[66:81], v[124:127], v[116:119], v[66:81]
	ds_read_b128 v[148:151], v108 offset:30720
	v_mfma_f32_32x32x16_f16 v[18:33], v[128:131], v[116:119], v[18:33]
	ds_read_b128 v[136:139], v106 offset:30720
	v_mfma_f32_32x32x16_f16 v[50:65], v[124:127], v[120:123], v[50:65]
	ds_read_b128 v[140:143], v106 offset:32768
	v_mfma_f32_32x32x16_f16 v[2:17], v[128:131], v[120:123], v[2:17]
	s_waitcnt lgkmcnt(0)
	v_mfma_f32_32x32x16_f16 v[82:97], v[144:147], v[132:135], v[82:97]
	v_mfma_f32_32x32x16_f16 v[34:49], v[148:151], v[132:135], v[34:49]
	v_mfma_f32_32x32x16_f16 v[66:81], v[144:147], v[136:139], v[66:81]
	v_mfma_f32_32x32x16_f16 v[18:33], v[148:151], v[136:139], v[18:33]
	v_mfma_f32_32x32x16_f16 v[50:65], v[144:147], v[140:143], v[50:65]
	v_mfma_f32_32x32x16_f16 v[2:17], v[148:151], v[140:143], v[2:17]

.LBB1_108:
	s_load_dwordx2 s[24:25], s[0:1], 0x38
	s_cmp_eq_u32 s3, 1
	s_cselect_b32 s4, s10, s12
	s_cselect_b32 s5, s11, s13
	s_cselect_b32 s6, s16, s14
	s_cselect_b32 s7, s17, s15
	s_cmp_eq_u32 s3, 2
	s_cselect_b32 s4, s8, s4
	s_cselect_b32 s5, s9, s5
	s_cselect_b32 s19, 0x3e38aa3b, 1.0
	s_lshr_b32 s23, s22, 3
	s_and_b32 s26, s21, 0x700
	s_waitcnt lgkmcnt(0)
	s_barrier
	s_cmp_lt_u32 s2, 64
	s_cbranch_scc1 .Lqkv_out_v
	s_mov_b32 s27, 0xaaaaaab
	v_mul_hi_u32 v1, v0, s27
	v_mul_u32_u24_e32 v2, 24, v1
	v_sub_u32_e32 v2, v0, v2
	v_lshl_add_u32 v3, v2, 3, s20
	v_lshlrev_b32_e32 v4, 2, v3
	global_load_dwordx4 v[8:11], v4, s[4:5]
	global_load_dwordx4 v[12:15], v4, s[4:5] offset:16
	v_mul_u32_u24_e32 v5, 0x190, v1
	v_lshl_add_u32 v5, v2, 4, v5
	v_add_u32_e32 v6, 0xc800, v5
	ds_read_b128 v[16:19], v5
	ds_read_b128 v[20:23], v5 offset:12800
	ds_read_b128 v[24:27], v5 offset:25600
	ds_read_b128 v[28:31], v5 offset:38400
	ds_read_b128 v[32:35], v6
	ds_read_b128 v[36:39], v6 offset:12800
	ds_read_b128 v[40:43], v6 offset:25600
	ds_read_b128 v[44:47], v6 offset:38400
	v_lshrrev_b32_e32 v7, 6, v3
	s_mul_i32 s27, s23, 12
	v_add_u32_e32 v7, s27, v7
	v_lshlrev_b32_e32 v7, 18, v7
	v_and_b32_e32 v48, 63, v3
	v_lshlrev_b32_e32 v48, 1, v48
	v_add_u32_e32 v49, s26, v1
	v_lshl_add_u32 v48, v49, 7, v48
	v_add_u32_e32 v7, v7, v48
	s_waitcnt vmcnt(0)
	s_waitcnt lgkmcnt(7)
	v_cvt_f32_f16_e32 v50, v16
	v_cvt_f32_f16_sdwa v51, v16 dst_sel:DWORD dst_unused:UNUSED_PAD src0_sel:WORD_1
	v_cvt_f32_f16_e32 v52, v17
	v_cvt_f32_f16_sdwa v53, v17 dst_sel:DWORD dst_unused:UNUSED_PAD src0_sel:WORD_1
	v_cvt_f32_f16_e32 v54, v18
	v_cvt_f32_f16_sdwa v55, v18 dst_sel:DWORD dst_unused:UNUSED_PAD src0_sel:WORD_1
	v_cvt_f32_f16_e32 v56, v19
	v_cvt_f32_f16_sdwa v57, v19 dst_sel:DWORD dst_unused:UNUSED_PAD src0_sel:WORD_1
	v_add_f32_e32 v50, v50, v8
	v_add_f32_e32 v51, v51, v9
	v_add_f32_e32 v52, v52, v10
	v_add_f32_e32 v53, v53, v11
	v_add_f32_e32 v54, v54, v12
	v_add_f32_e32 v55, v55, v13
	v_add_f32_e32 v56, v56, v14
	v_add_f32_e32 v57, v57, v15
	v_mul_f32_e32 v50, s19, v50
	v_mul_f32_e32 v51, s19, v51
	v_mul_f32_e32 v52, s19, v52
	v_mul_f32_e32 v53, s19, v53
	v_mul_f32_e32 v54, s19, v54
	v_mul_f32_e32 v55, s19, v55
	v_mul_f32_e32 v56, s19, v56
	v_mul_f32_e32 v57, s19, v57
	v_cvt_pk_f16_f32 v58, v50, v51
	v_cvt_pk_f16_f32 v59, v52, v53
	v_cvt_pk_f16_f32 v60, v54, v55
	v_cvt_pk_f16_f32 v61, v56, v57
	global_store_dwordx4 v7, v[58:61], s[6:7]
	v_add_u32_e32 v7, 0x1000, v7
	s_waitcnt lgkmcnt(6)
	v_cvt_f32_f16_e32 v50, v20
	v_cvt_f32_f16_sdwa v51, v20 dst_sel:DWORD dst_unused:UNUSED_PAD src0_sel:WORD_1
	v_cvt_f32_f16_e32 v52, v21
	v_cvt_f32_f16_sdwa v53, v21 dst_sel:DWORD dst_unused:UNUSED_PAD src0_sel:WORD_1
	v_cvt_f32_f16_e32 v54, v22
	v_cvt_f32_f16_sdwa v55, v22 dst_sel:DWORD dst_unused:UNUSED_PAD src0_sel:WORD_1
	v_cvt_f32_f16_e32 v56, v23
	v_cvt_f32_f16_sdwa v57, v23 dst_sel:DWORD dst_unused:UNUSED_PAD src0_sel:WORD_1
	v_add_f32_e32 v50, v50, v8
	v_add_f32_e32 v51, v51, v9
	v_add_f32_e32 v52, v52, v10
	v_add_f32_e32 v53, v53, v11
	v_add_f32_e32 v54, v54, v12
	v_add_f32_e32 v55, v55, v13
	v_add_f32_e32 v56, v56, v14
	v_add_f32_e32 v57, v57, v15
	v_mul_f32_e32 v50, s19, v50
	v_mul_f32_e32 v51, s19, v51
	v_mul_f32_e32 v52, s19, v52
	v_mul_f32_e32 v53, s19, v53
	v_mul_f32_e32 v54, s19, v54
	v_mul_f32_e32 v55, s19, v55
	v_mul_f32_e32 v56, s19, v56
	v_mul_f32_e32 v57, s19, v57
	v_cvt_pk_f16_f32 v58, v50, v51
	v_cvt_pk_f16_f32 v59, v52, v53
	v_cvt_pk_f16_f32 v60, v54, v55
	v_cvt_pk_f16_f32 v61, v56, v57
	global_store_dwordx4 v7, v[58:61], s[6:7]
	v_add_u32_e32 v7, 0x1000, v7
	s_waitcnt lgkmcnt(5)
	v_cvt_f32_f16_e32 v50, v24
	v_cvt_f32_f16_sdwa v51, v24 dst_sel:DWORD dst_unused:UNUSED_PAD src0_sel:WORD_1
	v_cvt_f32_f16_e32 v52, v25
	v_cvt_f32_f16_sdwa v53, v25 dst_sel:DWORD dst_unused:UNUSED_PAD src0_sel:WORD_1
	v_cvt_f32_f16_e32 v54, v26
	v_cvt_f32_f16_sdwa v55, v26 dst_sel:DWORD dst_unused:UNUSED_PAD src0_sel:WORD_1
	v_cvt_f32_f16_e32 v56, v27
	v_cvt_f32_f16_sdwa v57, v27 dst_sel:DWORD dst_unused:UNUSED_PAD src0_sel:WORD_1
	v_add_f32_e32 v50, v50, v8
	v_add_f32_e32 v51, v51, v9
	v_add_f32_e32 v52, v52, v10
	v_add_f32_e32 v53, v53, v11
	v_add_f32_e32 v54, v54, v12
	v_add_f32_e32 v55, v55, v13
	v_add_f32_e32 v56, v56, v14
	v_add_f32_e32 v57, v57, v15
	v_mul_f32_e32 v50, s19, v50
	v_mul_f32_e32 v51, s19, v51
	v_mul_f32_e32 v52, s19, v52
	v_mul_f32_e32 v53, s19, v53
	v_mul_f32_e32 v54, s19, v54
	v_mul_f32_e32 v55, s19, v55
	v_mul_f32_e32 v56, s19, v56
	v_mul_f32_e32 v57, s19, v57
	v_cvt_pk_f16_f32 v58, v50, v51
	v_cvt_pk_f16_f32 v59, v52, v53
	v_cvt_pk_f16_f32 v60, v54, v55
	v_cvt_pk_f16_f32 v61, v56, v57
	global_store_dwordx4 v7, v[58:61], s[6:7]
	v_add_u32_e32 v7, 0x1000, v7
	s_waitcnt lgkmcnt(4)
	v_cvt_f32_f16_e32 v50, v28
	v_cvt_f32_f16_sdwa v51, v28 dst_sel:DWORD dst_unused:UNUSED_PAD src0_sel:WORD_1
	v_cvt_f32_f16_e32 v52, v29
	v_cvt_f32_f16_sdwa v53, v29 dst_sel:DWORD dst_unused:UNUSED_PAD src0_sel:WORD_1
	v_cvt_f32_f16_e32 v54, v30
	v_cvt_f32_f16_sdwa v55, v30 dst_sel:DWORD dst_unused:UNUSED_PAD src0_sel:WORD_1
	v_cvt_f32_f16_e32 v56, v31
	v_cvt_f32_f16_sdwa v57, v31 dst_sel:DWORD dst_unused:UNUSED_PAD src0_sel:WORD_1
	v_add_f32_e32 v50, v50, v8
	v_add_f32_e32 v51, v51, v9
	v_add_f32_e32 v52, v52, v10
	v_add_f32_e32 v53, v53, v11
	v_add_f32_e32 v54, v54, v12
	v_add_f32_e32 v55, v55, v13
	v_add_f32_e32 v56, v56, v14
	v_add_f32_e32 v57, v57, v15
	v_mul_f32_e32 v50, s19, v50
	v_mul_f32_e32 v51, s19, v51
	v_mul_f32_e32 v52, s19, v52
	v_mul_f32_e32 v53, s19, v53
	v_mul_f32_e32 v54, s19, v54
	v_mul_f32_e32 v55, s19, v55
	v_mul_f32_e32 v56, s19, v56
	v_mul_f32_e32 v57, s19, v57
	v_cvt_pk_f16_f32 v58, v50, v51
	v_cvt_pk_f16_f32 v59, v52, v53
	v_cvt_pk_f16_f32 v60, v54, v55
	v_cvt_pk_f16_f32 v61, v56, v57
	global_store_dwordx4 v7, v[58:61], s[6:7]
	v_add_u32_e32 v7, 0x1000, v7
	s_waitcnt lgkmcnt(3)
	v_cvt_f32_f16_e32 v50, v32
	v_cvt_f32_f16_sdwa v51, v32 dst_sel:DWORD dst_unused:UNUSED_PAD src0_sel:WORD_1
	v_cvt_f32_f16_e32 v52, v33
	v_cvt_f32_f16_sdwa v53, v33 dst_sel:DWORD dst_unused:UNUSED_PAD src0_sel:WORD_1
	v_cvt_f32_f16_e32 v54, v34
	v_cvt_f32_f16_sdwa v55, v34 dst_sel:DWORD dst_unused:UNUSED_PAD src0_sel:WORD_1
	v_cvt_f32_f16_e32 v56, v35
	v_cvt_f32_f16_sdwa v57, v35 dst_sel:DWORD dst_unused:UNUSED_PAD src0_sel:WORD_1
	v_add_f32_e32 v50, v50, v8
	v_add_f32_e32 v51, v51, v9
	v_add_f32_e32 v52, v52, v10
	v_add_f32_e32 v53, v53, v11
	v_add_f32_e32 v54, v54, v12
	v_add_f32_e32 v55, v55, v13
	v_add_f32_e32 v56, v56, v14
	v_add_f32_e32 v57, v57, v15
	v_mul_f32_e32 v50, s19, v50
	v_mul_f32_e32 v51, s19, v51
	v_mul_f32_e32 v52, s19, v52
	v_mul_f32_e32 v53, s19, v53
	v_mul_f32_e32 v54, s19, v54
	v_mul_f32_e32 v55, s19, v55
	v_mul_f32_e32 v56, s19, v56
	v_mul_f32_e32 v57, s19, v57
	v_cvt_pk_f16_f32 v58, v50, v51
	v_cvt_pk_f16_f32 v59, v52, v53
	v_cvt_pk_f16_f32 v60, v54, v55
	v_cvt_pk_f16_f32 v61, v56, v57
	global_store_dwordx4 v7, v[58:61], s[6:7]
	v_add_u32_e32 v7, 0x1000, v7
	s_waitcnt lgkmcnt(2)
	v_cvt_f32_f16_e32 v50, v36
	v_cvt_f32_f16_sdwa v51, v36 dst_sel:DWORD dst_unused:UNUSED_PAD src0_sel:WORD_1
	v_cvt_f32_f16_e32 v52, v37
	v_cvt_f32_f16_sdwa v53, v37 dst_sel:DWORD dst_unused:UNUSED_PAD src0_sel:WORD_1
	v_cvt_f32_f16_e32 v54, v38
	v_cvt_f32_f16_sdwa v55, v38 dst_sel:DWORD dst_unused:UNUSED_PAD src0_sel:WORD_1
	v_cvt_f32_f16_e32 v56, v39
	v_cvt_f32_f16_sdwa v57, v39 dst_sel:DWORD dst_unused:UNUSED_PAD src0_sel:WORD_1
	v_add_f32_e32 v50, v50, v8
	v_add_f32_e32 v51, v51, v9
	v_add_f32_e32 v52, v52, v10
	v_add_f32_e32 v53, v53, v11
	v_add_f32_e32 v54, v54, v12
	v_add_f32_e32 v55, v55, v13
	v_add_f32_e32 v56, v56, v14
	v_add_f32_e32 v57, v57, v15
	v_mul_f32_e32 v50, s19, v50
	v_mul_f32_e32 v51, s19, v51
	v_mul_f32_e32 v52, s19, v52
	v_mul_f32_e32 v53, s19, v53
	v_mul_f32_e32 v54, s19, v54
	v_mul_f32_e32 v55, s19, v55
	v_mul_f32_e32 v56, s19, v56
	v_mul_f32_e32 v57, s19, v57
	v_cvt_pk_f16_f32 v58, v50, v51
	v_cvt_pk_f16_f32 v59, v52, v53
	v_cvt_pk_f16_f32 v60, v54, v55
	v_cvt_pk_f16_f32 v61, v56, v57
	global_store_dwordx4 v7, v[58:61], s[6:7]
	v_add_u32_e32 v7, 0x1000, v7
	s_waitcnt lgkmcnt(1)
	v_cvt_f32_f16_e32 v50, v40
	v_cvt_f32_f16_sdwa v51, v40 dst_sel:DWORD dst_unused:UNUSED_PAD src0_sel:WORD_1
	v_cvt_f32_f16_e32 v52, v41
	v_cvt_f32_f16_sdwa v53, v41 dst_sel:DWORD dst_unused:UNUSED_PAD src0_sel:WORD_1
	v_cvt_f32_f16_e32 v54, v42
	v_cvt_f32_f16_sdwa v55, v42 dst_sel:DWORD dst_unused:UNUSED_PAD src0_sel:WORD_1
	v_cvt_f32_f16_e32 v56, v43
	v_cvt_f32_f16_sdwa v57, v43 dst_sel:DWORD dst_unused:UNUSED_PAD src0_sel:WORD_1
	v_add_f32_e32 v50, v50, v8
	v_add_f32_e32 v51, v51, v9
	v_add_f32_e32 v52, v52, v10
	v_add_f32_e32 v53, v53, v11
	v_add_f32_e32 v54, v54, v12
	v_add_f32_e32 v55, v55, v13
	v_add_f32_e32 v56, v56, v14
	v_add_f32_e32 v57, v57, v15
	v_mul_f32_e32 v50, s19, v50
	v_mul_f32_e32 v51, s19, v51
	v_mul_f32_e32 v52, s19, v52
	v_mul_f32_e32 v53, s19, v53
	v_mul_f32_e32 v54, s19, v54
	v_mul_f32_e32 v55, s19, v55
	v_mul_f32_e32 v56, s19, v56
	v_mul_f32_e32 v57, s19, v57
	v_cvt_pk_f16_f32 v58, v50, v51
	v_cvt_pk_f16_f32 v59, v52, v53
	v_cvt_pk_f16_f32 v60, v54, v55
	v_cvt_pk_f16_f32 v61, v56, v57
	global_store_dwordx4 v7, v[58:61], s[6:7]
	v_add_u32_e32 v7, 0x1000, v7
	s_waitcnt lgkmcnt(0)
	v_cvt_f32_f16_e32 v50, v44
	v_cvt_f32_f16_sdwa v51, v44 dst_sel:DWORD dst_unused:UNUSED_PAD src0_sel:WORD_1
	v_cvt_f32_f16_e32 v52, v45
	v_cvt_f32_f16_sdwa v53, v45 dst_sel:DWORD dst_unused:UNUSED_PAD src0_sel:WORD_1
	v_cvt_f32_f16_e32 v54, v46
	v_cvt_f32_f16_sdwa v55, v46 dst_sel:DWORD dst_unused:UNUSED_PAD src0_sel:WORD_1
	v_cvt_f32_f16_e32 v56, v47
	v_cvt_f32_f16_sdwa v57, v47 dst_sel:DWORD dst_unused:UNUSED_PAD src0_sel:WORD_1
	v_add_f32_e32 v50, v50, v8
	v_add_f32_e32 v51, v51, v9
	v_add_f32_e32 v52, v52, v10
	v_add_f32_e32 v53, v53, v11
	v_add_f32_e32 v54, v54, v12
	v_add_f32_e32 v55, v55, v13
	v_add_f32_e32 v56, v56, v14
	v_add_f32_e32 v57, v57, v15
	v_mul_f32_e32 v50, s19, v50
	v_mul_f32_e32 v51, s19, v51
	v_mul_f32_e32 v52, s19, v52
	v_mul_f32_e32 v53, s19, v53
	v_mul_f32_e32 v54, s19, v54
	v_mul_f32_e32 v55, s19, v55
	v_mul_f32_e32 v56, s19, v56
	v_mul_f32_e32 v57, s19, v57
	v_cvt_pk_f16_f32 v58, v50, v51
	v_cvt_pk_f16_f32 v59, v52, v53
	v_cvt_pk_f16_f32 v60, v54, v55
	v_cvt_pk_f16_f32 v61, v56, v57
	global_store_dwordx4 v7, v[58:61], s[6:7]
	s_endpgm
.Lqkv_out_v:
	v_lshrrev_b32_e32 v1, 5, v0
	v_and_b32_e32 v2, 31, v0
	v_add_u32_e32 v3, s20, v1
	v_lshlrev_b32_e32 v4, 2, v3
	global_load_dword v8, v4, s[4:5]
	global_load_dword v9, v4, s[4:5] offset:96
	global_load_dword v10, v4, s[4:5] offset:192
	global_load_dword v11, v4, s[4:5] offset:288
	global_load_dword v12, v4, s[4:5] offset:384
	global_load_dword v13, v4, s[4:5] offset:480
	global_load_dword v14, v4, s[4:5] offset:576
	global_load_dword v15, v4, s[4:5] offset:672
	v_mul_u32_u24_e32 v5, 0x210, v1
	v_lshl_add_u32 v5, v2, 4, v5
	v_add_u32_e32 v6, 0xc600, v5
	ds_read_b128 v[16:19], v5
	ds_read_b128 v[20:23], v5 offset:12672
	ds_read_b128 v[24:27], v5 offset:25344
	ds_read_b128 v[28:31], v5 offset:38016
	ds_read_b128 v[32:35], v6
	ds_read_b128 v[36:39], v6 offset:12672
	ds_read_b128 v[40:43], v6 offset:25344
	ds_read_b128 v[44:47], v6 offset:38016
	s_mul_i32 s27, s23, 0x300
	v_add_u32_e32 v7, s27, v3
	v_lshlrev_b32_e32 v7, 12, v7
	v_lshl_add_u32 v48, v2, 3, s26
	v_lshl_add_u32 v7, v48, 1, v7
	s_waitcnt vmcnt(7) lgkmcnt(7)
	v_cvt_f32_f16_e32 v50, v16
	v_cvt_f32_f16_sdwa v51, v16 dst_sel:DWORD dst_unused:UNUSED_PAD src0_sel:WORD_1
	v_cvt_f32_f16_e32 v52, v17
	v_cvt_f32_f16_sdwa v53, v17 dst_sel:DWORD dst_unused:UNUSED_PAD src0_sel:WORD_1
	v_cvt_f32_f16_e32 v54, v18
	v_cvt_f32_f16_sdwa v55, v18 dst_sel:DWORD dst_unused:UNUSED_PAD src0_sel:WORD_1
	v_cvt_f32_f16_e32 v56, v19
	v_cvt_f32_f16_sdwa v57, v19 dst_sel:DWORD dst_unused:UNUSED_PAD src0_sel:WORD_1
	v_add_f32_e32 v50, v50, v8
	v_add_f32_e32 v51, v51, v8
	v_add_f32_e32 v52, v52, v8
	v_add_f32_e32 v53, v53, v8
	v_add_f32_e32 v54, v54, v8
	v_add_f32_e32 v55, v55, v8
	v_add_f32_e32 v56, v56, v8
	v_add_f32_e32 v57, v57, v8
	v_cvt_pk_f16_f32 v58, v50, v51
	v_cvt_pk_f16_f32 v59, v52, v53
	v_cvt_pk_f16_f32 v60, v54, v55
	v_cvt_pk_f16_f32 v61, v56, v57
	global_store_dwordx4 v7, v[58:61], s[24:25]
	v_add_u32_e32 v7, 0x18000, v7
	s_waitcnt vmcnt(7) lgkmcnt(6)
	v_cvt_f32_f16_e32 v50, v20
	v_cvt_f32_f16_sdwa v51, v20 dst_sel:DWORD dst_unused:UNUSED_PAD src0_sel:WORD_1
	v_cvt_f32_f16_e32 v52, v21
	v_cvt_f32_f16_sdwa v53, v21 dst_sel:DWORD dst_unused:UNUSED_PAD src0_sel:WORD_1
	v_cvt_f32_f16_e32 v54, v22
	v_cvt_f32_f16_sdwa v55, v22 dst_sel:DWORD dst_unused:UNUSED_PAD src0_sel:WORD_1
	v_cvt_f32_f16_e32 v56, v23
	v_cvt_f32_f16_sdwa v57, v23 dst_sel:DWORD dst_unused:UNUSED_PAD src0_sel:WORD_1
	v_add_f32_e32 v50, v50, v9
	v_add_f32_e32 v51, v51, v9
	v_add_f32_e32 v52, v52, v9
	v_add_f32_e32 v53, v53, v9
	v_add_f32_e32 v54, v54, v9
	v_add_f32_e32 v55, v55, v9
	v_add_f32_e32 v56, v56, v9
	v_add_f32_e32 v57, v57, v9
	v_cvt_pk_f16_f32 v58, v50, v51
	v_cvt_pk_f16_f32 v59, v52, v53
	v_cvt_pk_f16_f32 v60, v54, v55
	v_cvt_pk_f16_f32 v61, v56, v57
	global_store_dwordx4 v7, v[58:61], s[24:25]
	v_add_u32_e32 v7, 0x18000, v7
	s_waitcnt vmcnt(7) lgkmcnt(5)
	v_cvt_f32_f16_e32 v50, v24
	v_cvt_f32_f16_sdwa v51, v24 dst_sel:DWORD dst_unused:UNUSED_PAD src0_sel:WORD_1
	v_cvt_f32_f16_e32 v52, v25
	v_cvt_f32_f16_sdwa v53, v25 dst_sel:DWORD dst_unused:UNUSED_PAD src0_sel:WORD_1
	v_cvt_f32_f16_e32 v54, v26
	v_cvt_f32_f16_sdwa v55, v26 dst_sel:DWORD dst_unused:UNUSED_PAD src0_sel:WORD_1
	v_cvt_f32_f16_e32 v56, v27
	v_cvt_f32_f16_sdwa v57, v27 dst_sel:DWORD dst_unused:UNUSED_PAD src0_sel:WORD_1
	v_add_f32_e32 v50, v50, v10
	v_add_f32_e32 v51, v51, v10
	v_add_f32_e32 v52, v52, v10
	v_add_f32_e32 v53, v53, v10
	v_add_f32_e32 v54, v54, v10
	v_add_f32_e32 v55, v55, v10
	v_add_f32_e32 v56, v56, v10
	v_add_f32_e32 v57, v57, v10
	v_cvt_pk_f16_f32 v58, v50, v51
	v_cvt_pk_f16_f32 v59, v52, v53
	v_cvt_pk_f16_f32 v60, v54, v55
	v_cvt_pk_f16_f32 v61, v56, v57
	global_store_dwordx4 v7, v[58:61], s[24:25]
	v_add_u32_e32 v7, 0x18000, v7
	s_waitcnt vmcnt(7) lgkmcnt(4)
	v_cvt_f32_f16_e32 v50, v28
	v_cvt_f32_f16_sdwa v51, v28 dst_sel:DWORD dst_unused:UNUSED_PAD src0_sel:WORD_1
	v_cvt_f32_f16_e32 v52, v29
	v_cvt_f32_f16_sdwa v53, v29 dst_sel:DWORD dst_unused:UNUSED_PAD src0_sel:WORD_1
	v_cvt_f32_f16_e32 v54, v30
	v_cvt_f32_f16_sdwa v55, v30 dst_sel:DWORD dst_unused:UNUSED_PAD src0_sel:WORD_1
	v_cvt_f32_f16_e32 v56, v31
	v_cvt_f32_f16_sdwa v57, v31 dst_sel:DWORD dst_unused:UNUSED_PAD src0_sel:WORD_1
	v_add_f32_e32 v50, v50, v11
	v_add_f32_e32 v51, v51, v11
	v_add_f32_e32 v52, v52, v11
	v_add_f32_e32 v53, v53, v11
	v_add_f32_e32 v54, v54, v11
	v_add_f32_e32 v55, v55, v11
	v_add_f32_e32 v56, v56, v11
	v_add_f32_e32 v57, v57, v11
	v_cvt_pk_f16_f32 v58, v50, v51
	v_cvt_pk_f16_f32 v59, v52, v53
	v_cvt_pk_f16_f32 v60, v54, v55
	v_cvt_pk_f16_f32 v61, v56, v57
	global_store_dwordx4 v7, v[58:61], s[24:25]
	v_add_u32_e32 v7, 0x18000, v7
	s_waitcnt vmcnt(7) lgkmcnt(3)
	v_cvt_f32_f16_e32 v50, v32
	v_cvt_f32_f16_sdwa v51, v32 dst_sel:DWORD dst_unused:UNUSED_PAD src0_sel:WORD_1
	v_cvt_f32_f16_e32 v52, v33
	v_cvt_f32_f16_sdwa v53, v33 dst_sel:DWORD dst_unused:UNUSED_PAD src0_sel:WORD_1
	v_cvt_f32_f16_e32 v54, v34
	v_cvt_f32_f16_sdwa v55, v34 dst_sel:DWORD dst_unused:UNUSED_PAD src0_sel:WORD_1
	v_cvt_f32_f16_e32 v56, v35
	v_cvt_f32_f16_sdwa v57, v35 dst_sel:DWORD dst_unused:UNUSED_PAD src0_sel:WORD_1
	v_add_f32_e32 v50, v50, v12
	v_add_f32_e32 v51, v51, v12
	v_add_f32_e32 v52, v52, v12
	v_add_f32_e32 v53, v53, v12
	v_add_f32_e32 v54, v54, v12
	v_add_f32_e32 v55, v55, v12
	v_add_f32_e32 v56, v56, v12
	v_add_f32_e32 v57, v57, v12
	v_cvt_pk_f16_f32 v58, v50, v51
	v_cvt_pk_f16_f32 v59, v52, v53
	v_cvt_pk_f16_f32 v60, v54, v55
	v_cvt_pk_f16_f32 v61, v56, v57
	global_store_dwordx4 v7, v[58:61], s[24:25]
	v_add_u32_e32 v7, 0x18000, v7
	s_waitcnt vmcnt(7) lgkmcnt(2)
	v_cvt_f32_f16_e32 v50, v36
	v_cvt_f32_f16_sdwa v51, v36 dst_sel:DWORD dst_unused:UNUSED_PAD src0_sel:WORD_1
	v_cvt_f32_f16_e32 v52, v37
	v_cvt_f32_f16_sdwa v53, v37 dst_sel:DWORD dst_unused:UNUSED_PAD src0_sel:WORD_1
	v_cvt_f32_f16_e32 v54, v38
	v_cvt_f32_f16_sdwa v55, v38 dst_sel:DWORD dst_unused:UNUSED_PAD src0_sel:WORD_1
	v_cvt_f32_f16_e32 v56, v39
	v_cvt_f32_f16_sdwa v57, v39 dst_sel:DWORD dst_unused:UNUSED_PAD src0_sel:WORD_1
	v_add_f32_e32 v50, v50, v13
	v_add_f32_e32 v51, v51, v13
	v_add_f32_e32 v52, v52, v13
	v_add_f32_e32 v53, v53, v13
	v_add_f32_e32 v54, v54, v13
	v_add_f32_e32 v55, v55, v13
	v_add_f32_e32 v56, v56, v13
	v_add_f32_e32 v57, v57, v13
	v_cvt_pk_f16_f32 v58, v50, v51
	v_cvt_pk_f16_f32 v59, v52, v53
	v_cvt_pk_f16_f32 v60, v54, v55
	v_cvt_pk_f16_f32 v61, v56, v57
	global_store_dwordx4 v7, v[58:61], s[24:25]
	v_add_u32_e32 v7, 0x18000, v7
	s_waitcnt vmcnt(7) lgkmcnt(1)
	v_cvt_f32_f16_e32 v50, v40
	v_cvt_f32_f16_sdwa v51, v40 dst_sel:DWORD dst_unused:UNUSED_PAD src0_sel:WORD_1
	v_cvt_f32_f16_e32 v52, v41
	v_cvt_f32_f16_sdwa v53, v41 dst_sel:DWORD dst_unused:UNUSED_PAD src0_sel:WORD_1
	v_cvt_f32_f16_e32 v54, v42
	v_cvt_f32_f16_sdwa v55, v42 dst_sel:DWORD dst_unused:UNUSED_PAD src0_sel:WORD_1
	v_cvt_f32_f16_e32 v56, v43
	v_cvt_f32_f16_sdwa v57, v43 dst_sel:DWORD dst_unused:UNUSED_PAD src0_sel:WORD_1
	v_add_f32_e32 v50, v50, v14
	v_add_f32_e32 v51, v51, v14
	v_add_f32_e32 v52, v52, v14
	v_add_f32_e32 v53, v53, v14
	v_add_f32_e32 v54, v54, v14
	v_add_f32_e32 v55, v55, v14
	v_add_f32_e32 v56, v56, v14
	v_add_f32_e32 v57, v57, v14
	v_cvt_pk_f16_f32 v58, v50, v51
	v_cvt_pk_f16_f32 v59, v52, v53
	v_cvt_pk_f16_f32 v60, v54, v55
	v_cvt_pk_f16_f32 v61, v56, v57
	global_store_dwordx4 v7, v[58:61], s[24:25]
	v_add_u32_e32 v7, 0x18000, v7
	s_waitcnt vmcnt(7) lgkmcnt(0)
	v_cvt_f32_f16_e32 v50, v44
	v_cvt_f32_f16_sdwa v51, v44 dst_sel:DWORD dst_unused:UNUSED_PAD src0_sel:WORD_1
	v_cvt_f32_f16_e32 v52, v45
	v_cvt_f32_f16_sdwa v53, v45 dst_sel:DWORD dst_unused:UNUSED_PAD src0_sel:WORD_1
	v_cvt_f32_f16_e32 v54, v46
	v_cvt_f32_f16_sdwa v55, v46 dst_sel:DWORD dst_unused:UNUSED_PAD src0_sel:WORD_1
	v_cvt_f32_f16_e32 v56, v47
	v_cvt_f32_f16_sdwa v57, v47 dst_sel:DWORD dst_unused:UNUSED_PAD src0_sel:WORD_1
	v_add_f32_e32 v50, v50, v15
	v_add_f32_e32 v51, v51, v15
	v_add_f32_e32 v52, v52, v15
	v_add_f32_e32 v53, v53, v15
	v_add_f32_e32 v54, v54, v15
	v_add_f32_e32 v55, v55, v15
	v_add_f32_e32 v56, v56, v15
	v_add_f32_e32 v57, v57, v15
	v_cvt_pk_f16_f32 v58, v50, v51
	v_cvt_pk_f16_f32 v59, v52, v53
	v_cvt_pk_f16_f32 v60, v54, v55
	v_cvt_pk_f16_f32 v61, v56, v57
	global_store_dwordx4 v7, v[58:61], s[24:25]
	s_endpgm

	.amdhsa_kernel _Z15qkv_proj_kernelPKDF16_S0_PKfS2_S2_PDF16_S3_S3_
		.amdhsa_group_segment_fixed_size 0
		.amdhsa_private_segment_fixed_size 0
		.amdhsa_kernarg_size 64
		.amdhsa_user_sgpr_count 2
		.amdhsa_user_sgpr_dispatch_ptr 0
		.amdhsa_user_sgpr_queue_ptr 0
		.amdhsa_user_sgpr_kernarg_segment_ptr 1
		.amdhsa_user_sgpr_dispatch_id 0
		.amdhsa_user_sgpr_kernarg_preload_length 0
		.amdhsa_user_sgpr_kernarg_preload_offset 0
		.amdhsa_user_sgpr_private_segment_size 0
		.amdhsa_uses_dynamic_stack 0
		.amdhsa_enable_private_segment 0
		.amdhsa_system_sgpr_workgroup_id_x 1
		.amdhsa_system_sgpr_workgroup_id_y 0
		.amdhsa_system_sgpr_workgroup_id_z 0
		.amdhsa_system_sgpr_workgroup_info 0
		.amdhsa_system_vgpr_workitem_id 0
		.amdhsa_next_free_vgpr 152
		.amdhsa_next_free_sgpr 41
		.amdhsa_accum_offset 152
		.amdhsa_reserve_vcc 1
		.amdhsa_float_round_mode_32 0
		.amdhsa_float_round_mode_16_64 0
		.amdhsa_float_denorm_mode_32 3
		.amdhsa_float_denorm_mode_16_64 3
		.amdhsa_dx10_clamp 1
		.amdhsa_ieee_mode 1
		.amdhsa_fp16_overflow 0
		.amdhsa_tg_split 0
		.amdhsa_exception_fp_ieee_invalid_op 0
		.amdhsa_exception_fp_denorm_src 0
		.amdhsa_exception_fp_ieee_div_zero 0
		.amdhsa_exception_fp_ieee_overflow 0
		.amdhsa_exception_fp_ieee_underflow 0
		.amdhsa_exception_fp_ieee_inexact 0
		.amdhsa_exception_int_div_zero 0
	.end_amdhsa_kernel

.LBB2_3:
	s_load_dwordx4 s[4:7], s[0:1], 0x10
	v_and_b32_e32 v51, 31, v1
	v_lshrrev_b32_e32 v50, 5, v1
	v_bfe_u32 v52, v1, 1, 3
	s_lshl_b32 s2, s13, 5
	v_or_b32_e32 v53, s2, v51
	v_lshlrev_b32_e32 v53, 7, v53
	v_lshlrev_b32_e32 v54, 7, v51
	v_add_u32_e32 v54, 0x4000, v54
	v_xor_b32_e32 v55, v50, v52
	v_lshlrev_b32_e32 v104, 4, v55
	v_add_u32_e32 v56, v53, v104
	v_add_u32_e32 v60, v54, v104
	v_add_u32_e32 v64, 0xe000, v56
	v_add_u32_e32 v68, 0xe000, v60
	v_xor_b32_e32 v104, 2, v55
	v_lshlrev_b32_e32 v104, 4, v104
	v_add_u32_e32 v57, v53, v104
	v_add_u32_e32 v61, v54, v104
	v_add_u32_e32 v65, 0xe000, v57
	v_add_u32_e32 v69, 0xe000, v61
	v_xor_b32_e32 v104, 4, v55
	v_lshlrev_b32_e32 v104, 4, v104
	v_add_u32_e32 v58, v53, v104
	v_add_u32_e32 v62, v54, v104
	v_add_u32_e32 v66, 0xe000, v58
	v_add_u32_e32 v70, 0xe000, v62
	v_xor_b32_e32 v104, 6, v55
	v_lshlrev_b32_e32 v104, 4, v104
	v_add_u32_e32 v59, v53, v104
	v_add_u32_e32 v63, v54, v104
	v_add_u32_e32 v67, 0xe000, v59
	v_add_u32_e32 v71, 0xe000, v63
	v_mov_b32_e32 v2, 0
	v_mov_b32_e32 v3, 0
	v_mov_b32_e32 v4, 0
	v_mov_b32_e32 v5, 0
	v_mov_b32_e32 v6, 0
	v_mov_b32_e32 v7, 0
	v_mov_b32_e32 v8, 0
	v_mov_b32_e32 v9, 0
	v_mov_b32_e32 v10, 0
	v_mov_b32_e32 v11, 0
	v_mov_b32_e32 v12, 0
	v_mov_b32_e32 v13, 0
	v_mov_b32_e32 v14, 0
	v_mov_b32_e32 v15, 0
	v_mov_b32_e32 v16, 0
	v_mov_b32_e32 v17, 0
	v_mov_b32_e32 v18, 0
	v_mov_b32_e32 v19, 0
	v_mov_b32_e32 v20, 0
	v_mov_b32_e32 v21, 0
	v_mov_b32_e32 v22, 0
	v_mov_b32_e32 v23, 0
	v_mov_b32_e32 v24, 0
	v_mov_b32_e32 v25, 0
	v_mov_b32_e32 v26, 0
	v_mov_b32_e32 v27, 0
	v_mov_b32_e32 v28, 0
	v_mov_b32_e32 v29, 0
	v_mov_b32_e32 v30, 0
	v_mov_b32_e32 v31, 0
	v_mov_b32_e32 v32, 0
	v_mov_b32_e32 v33, 0
	v_mov_b32_e32 v34, 0
	v_mov_b32_e32 v35, 0
	v_mov_b32_e32 v36, 0
	v_mov_b32_e32 v37, 0
	v_mov_b32_e32 v38, 0
	v_mov_b32_e32 v39, 0
	v_mov_b32_e32 v40, 0
	v_mov_b32_e32 v41, 0
	v_mov_b32_e32 v42, 0
	v_mov_b32_e32 v43, 0
	v_mov_b32_e32 v44, 0
	v_mov_b32_e32 v45, 0
	v_mov_b32_e32 v46, 0
	v_mov_b32_e32 v47, 0
	v_mov_b32_e32 v48, 0
	v_mov_b32_e32 v49, 0
	s_barrier
	ds_read_b128 v[72:75], v56
	ds_read_b128 v[76:79], v60
	ds_read_b128 v[80:83], v60 offset:4096
	ds_read_b128 v[84:87], v60 offset:8192
	ds_read_b128 v[88:91], v57
	ds_read_b128 v[92:95], v61
	ds_read_b128 v[96:99], v61 offset:4096
	ds_read_b128 v[100:103], v61 offset:8192
	s_waitcnt lgkmcnt(0)
	v_mfma_f32_32x32x16_f16 v[34:49], v[72:75], v[76:79], v[34:49]
	ds_read_b128 v[104:107], v58
	ds_read_b128 v[108:111], v62
	v_mfma_f32_32x32x16_f16 v[18:33], v[72:75], v[80:83], v[18:33]
	ds_read_b128 v[112:115], v62 offset:4096
	ds_read_b128 v[116:119], v62 offset:8192
	v_mfma_f32_32x32x16_f16 v[2:17], v[72:75], v[84:87], v[2:17]
	ds_read_b128 v[120:123], v59
	v_mfma_f32_32x32x16_f16 v[34:49], v[88:91], v[92:95], v[34:49]
	ds_read_b128 v[124:127], v63
	v_mfma_f32_32x32x16_f16 v[18:33], v[88:91], v[96:99], v[18:33]
	ds_read_b128 v[128:131], v63 offset:4096
	v_mfma_f32_32x32x16_f16 v[2:17], v[88:91], v[100:103], v[2:17]
	ds_read_b128 v[132:135], v63 offset:8192
	s_waitcnt lgkmcnt(0)
	s_barrier
	v_mfma_f32_32x32x16_f16 v[34:49], v[104:107], v[108:111], v[34:49]
	ds_read_b128 v[72:75], v56 offset:28672
	ds_read_b128 v[76:79], v60 offset:28672
	v_mfma_f32_32x32x16_f16 v[18:33], v[104:107], v[112:115], v[18:33]
	ds_read_b128 v[80:83], v60 offset:32768
	ds_read_b128 v[84:87], v60 offset:36864
	v_mfma_f32_32x32x16_f16 v[2:17], v[104:107], v[116:119], v[2:17]
	ds_read_b128 v[88:91], v57 offset:28672
	v_mfma_f32_32x32x16_f16 v[34:49], v[120:123], v[124:127], v[34:49]
	ds_read_b128 v[92:95], v61 offset:28672
	v_mfma_f32_32x32x16_f16 v[18:33], v[120:123], v[128:131], v[18:33]
	ds_read_b128 v[96:99], v61 offset:32768
	v_mfma_f32_32x32x16_f16 v[2:17], v[120:123], v[132:135], v[2:17]
	ds_read_b128 v[100:103], v61 offset:36864
	s_waitcnt lgkmcnt(0)
	v_mfma_f32_32x32x16_f16 v[34:49], v[72:75], v[76:79], v[34:49]
	ds_read_b128 v[104:107], v58 offset:28672
	ds_read_b128 v[108:111], v62 offset:28672
	v_mfma_f32_32x32x16_f16 v[18:33], v[72:75], v[80:83], v[18:33]
	ds_read_b128 v[112:115], v62 offset:32768
	ds_read_b128 v[116:119], v62 offset:36864
	v_mfma_f32_32x32x16_f16 v[2:17], v[72:75], v[84:87], v[2:17]
	ds_read_b128 v[120:123], v59 offset:28672
	v_mfma_f32_32x32x16_f16 v[34:49], v[88:91], v[92:95], v[34:49]
	ds_read_b128 v[124:127], v63 offset:28672
	v_mfma_f32_32x32x16_f16 v[18:33], v[88:91], v[96:99], v[18:33]
	ds_read_b128 v[128:131], v63 offset:32768
	v_mfma_f32_32x32x16_f16 v[2:17], v[88:91], v[100:103], v[2:17]
	ds_read_b128 v[132:135], v63 offset:36864
	s_waitcnt lgkmcnt(0)
	s_barrier
	v_mfma_f32_32x32x16_f16 v[34:49], v[104:107], v[108:111], v[34:49]
	ds_read_b128 v[72:75], v64
	ds_read_b128 v[76:79], v68
	v_mfma_f32_32x32x16_f16 v[18:33], v[104:107], v[112:115], v[18:33]
	ds_read_b128 v[80:83], v68 offset:4096
	ds_read_b128 v[84:87], v68 offset:8192
	v_mfma_f32_32x32x16_f16 v[2:17], v[104:107], v[116:119], v[2:17]
	ds_read_b128 v[88:91], v65
	v_mfma_f32_32x32x16_f16 v[34:49], v[120:123], v[124:127], v[34:49]
	ds_read_b128 v[92:95], v69
	v_mfma_f32_32x32x16_f16 v[18:33], v[120:123], v[128:131], v[18:33]
	ds_read_b128 v[96:99], v69 offset:4096
	v_mfma_f32_32x32x16_f16 v[2:17], v[120:123], v[132:135], v[2:17]
	ds_read_b128 v[100:103], v69 offset:8192
	s_waitcnt lgkmcnt(0)
	v_mfma_f32_32x32x16_f16 v[34:49], v[72:75], v[76:79], v[34:49]
	ds_read_b128 v[104:107], v66
	ds_read_b128 v[108:111], v70
	v_mfma_f32_32x32x16_f16 v[18:33], v[72:75], v[80:83], v[18:33]
	ds_read_b128 v[112:115], v70 offset:4096
	ds_read_b128 v[116:119], v70 offset:8192
	v_mfma_f32_32x32x16_f16 v[2:17], v[72:75], v[84:87], v[2:17]
	ds_read_b128 v[120:123], v67
	v_mfma_f32_32x32x16_f16 v[34:49], v[88:91], v[92:95], v[34:49]
	ds_read_b128 v[124:127], v71
	v_mfma_f32_32x32x16_f16 v[18:33], v[88:91], v[96:99], v[18:33]
	ds_read_b128 v[128:131], v71 offset:4096
	v_mfma_f32_32x32x16_f16 v[2:17], v[88:91], v[100:103], v[2:17]
	ds_read_b128 v[132:135], v71 offset:8192
	s_waitcnt lgkmcnt(0)
	s_barrier
	v_mfma_f32_32x32x16_f16 v[34:49], v[104:107], v[108:111], v[34:49]
	ds_read_b128 v[72:75], v64 offset:28672
	ds_read_b128 v[76:79], v68 offset:28672
	v_mfma_f32_32x32x16_f16 v[18:33], v[104:107], v[112:115], v[18:33]
	ds_read_b128 v[80:83], v68 offset:32768
	ds_read_b128 v[84:87], v68 offset:36864
	v_mfma_f32_32x32x16_f16 v[2:17], v[104:107], v[116:119], v[2:17]
	ds_read_b128 v[88:91], v65 offset:28672
	v_mfma_f32_32x32x16_f16 v[34:49], v[120:123], v[124:127], v[34:49]
	ds_read_b128 v[92:95], v69 offset:28672
	v_mfma_f32_32x32x16_f16 v[18:33], v[120:123], v[128:131], v[18:33]
	ds_read_b128 v[96:99], v69 offset:32768
	v_mfma_f32_32x32x16_f16 v[2:17], v[120:123], v[132:135], v[2:17]
	ds_read_b128 v[100:103], v69 offset:36864
	s_waitcnt lgkmcnt(0)
	v_mfma_f32_32x32x16_f16 v[34:49], v[72:75], v[76:79], v[34:49]
	ds_read_b128 v[104:107], v66 offset:28672
	ds_read_b128 v[108:111], v70 offset:28672
	v_mfma_f32_32x32x16_f16 v[18:33], v[72:75], v[80:83], v[18:33]
	ds_read_b128 v[112:115], v70 offset:32768
	ds_read_b128 v[116:119], v70 offset:36864
	v_mfma_f32_32x32x16_f16 v[2:17], v[72:75], v[84:87], v[2:17]
	ds_read_b128 v[120:123], v67 offset:28672
	v_mfma_f32_32x32x16_f16 v[34:49], v[88:91], v[92:95], v[34:49]
	ds_read_b128 v[124:127], v71 offset:28672
	v_mfma_f32_32x32x16_f16 v[18:33], v[88:91], v[96:99], v[18:33]
	ds_read_b128 v[128:131], v71 offset:32768
	v_mfma_f32_32x32x16_f16 v[2:17], v[88:91], v[100:103], v[2:17]
	ds_read_b128 v[132:135], v71 offset:36864
	s_waitcnt lgkmcnt(0)
	s_barrier
	v_mfma_f32_32x32x16_f16 v[34:49], v[104:107], v[108:111], v[34:49]
	ds_read_b128 v[72:75], v56
	ds_read_b128 v[76:79], v60
	v_mfma_f32_32x32x16_f16 v[18:33], v[104:107], v[112:115], v[18:33]
	ds_read_b128 v[80:83], v60 offset:4096
	ds_read_b128 v[84:87], v60 offset:8192
	v_mfma_f32_32x32x16_f16 v[2:17], v[104:107], v[116:119], v[2:17]
	ds_read_b128 v[88:91], v57
	v_mfma_f32_32x32x16_f16 v[34:49], v[120:123], v[124:127], v[34:49]
	ds_read_b128 v[92:95], v61
	v_mfma_f32_32x32x16_f16 v[18:33], v[120:123], v[128:131], v[18:33]
	ds_read_b128 v[96:99], v61 offset:4096
	v_mfma_f32_32x32x16_f16 v[2:17], v[120:123], v[132:135], v[2:17]
	ds_read_b128 v[100:103], v61 offset:8192
	s_waitcnt lgkmcnt(0)
	v_mfma_f32_32x32x16_f16 v[34:49], v[72:75], v[76:79], v[34:49]
	ds_read_b128 v[104:107], v58
	ds_read_b128 v[108:111], v62
	v_mfma_f32_32x32x16_f16 v[18:33], v[72:75], v[80:83], v[18:33]
	ds_read_b128 v[112:115], v62 offset:4096
	ds_read_b128 v[116:119], v62 offset:8192
	v_mfma_f32_32x32x16_f16 v[2:17], v[72:75], v[84:87], v[2:17]
	ds_read_b128 v[120:123], v59
	v_mfma_f32_32x32x16_f16 v[34:49], v[88:91], v[92:95], v[34:49]
	ds_read_b128 v[124:127], v63
	v_mfma_f32_32x32x16_f16 v[18:33], v[88:91], v[96:99], v[18:33]
	ds_read_b128 v[128:131], v63 offset:4096
	v_mfma_f32_32x32x16_f16 v[2:17], v[88:91], v[100:103], v[2:17]
	ds_read_b128 v[132:135], v63 offset:8192
	s_waitcnt lgkmcnt(0)
	s_barrier
	v_mfma_f32_32x32x16_f16 v[34:49], v[104:107], v[108:111], v[34:49]
	ds_read_b128 v[72:75], v56 offset:28672
	ds_read_b128 v[76:79], v60 offset:28672
	v_mfma_f32_32x32x16_f16 v[18:33], v[104:107], v[112:115], v[18:33]
	ds_read_b128 v[80:83], v60 offset:32768
	ds_read_b128 v[84:87], v60 offset:36864
	v_mfma_f32_32x32x16_f16 v[2:17], v[104:107], v[116:119], v[2:17]
	ds_read_b128 v[88:91], v57 offset:28672
	v_mfma_f32_32x32x16_f16 v[34:49], v[120:123], v[124:127], v[34:49]
	ds_read_b128 v[92:95], v61 offset:28672
	v_mfma_f32_32x32x16_f16 v[18:33], v[120:123], v[128:131], v[18:33]
	ds_read_b128 v[96:99], v61 offset:32768
	v_mfma_f32_32x32x16_f16 v[2:17], v[120:123], v[132:135], v[2:17]
	ds_read_b128 v[100:103], v61 offset:36864
	s_waitcnt lgkmcnt(0)
	v_mfma_f32_32x32x16_f16 v[34:49], v[72:75], v[76:79], v[34:49]
	ds_read_b128 v[104:107], v58 offset:28672
	ds_read_b128 v[108:111], v62 offset:28672
	v_mfma_f32_32x32x16_f16 v[18:33], v[72:75], v[80:83], v[18:33]
	ds_read_b128 v[112:115], v62 offset:32768
	ds_read_b128 v[116:119], v62 offset:36864
	v_mfma_f32_32x32x16_f16 v[2:17], v[72:75], v[84:87], v[2:17]
	ds_read_b128 v[120:123], v59 offset:28672
	v_mfma_f32_32x32x16_f16 v[34:49], v[88:91], v[92:95], v[34:49]
	ds_read_b128 v[124:127], v63 offset:28672
	v_mfma_f32_32x32x16_f16 v[18:33], v[88:91], v[96:99], v[18:33]
	ds_read_b128 v[128:131], v63 offset:32768
	v_mfma_f32_32x32x16_f16 v[2:17], v[88:91], v[100:103], v[2:17]
	ds_read_b128 v[132:135], v63 offset:36864
	s_waitcnt lgkmcnt(0)
	s_barrier
	v_mfma_f32_32x32x16_f16 v[34:49], v[104:107], v[108:111], v[34:49]
	ds_read_b128 v[72:75], v64
	ds_read_b128 v[76:79], v68
	v_mfma_f32_32x32x16_f16 v[18:33], v[104:107], v[112:115], v[18:33]
	ds_read_b128 v[80:83], v68 offset:4096
	ds_read_b128 v[84:87], v68 offset:8192
	v_mfma_f32_32x32x16_f16 v[2:17], v[104:107], v[116:119], v[2:17]
	ds_read_b128 v[88:91], v65
	v_mfma_f32_32x32x16_f16 v[34:49], v[120:123], v[124:127], v[34:49]
	ds_read_b128 v[92:95], v69
	v_mfma_f32_32x32x16_f16 v[18:33], v[120:123], v[128:131], v[18:33]
	ds_read_b128 v[96:99], v69 offset:4096
	v_mfma_f32_32x32x16_f16 v[2:17], v[120:123], v[132:135], v[2:17]
	ds_read_b128 v[100:103], v69 offset:8192
	s_waitcnt lgkmcnt(0)
	v_mfma_f32_32x32x16_f16 v[34:49], v[72:75], v[76:79], v[34:49]
	ds_read_b128 v[104:107], v66
	ds_read_b128 v[108:111], v70
	v_mfma_f32_32x32x16_f16 v[18:33], v[72:75], v[80:83], v[18:33]
	ds_read_b128 v[112:115], v70 offset:4096
	ds_read_b128 v[116:119], v70 offset:8192
	v_mfma_f32_32x32x16_f16 v[2:17], v[72:75], v[84:87], v[2:17]
	ds_read_b128 v[120:123], v67
	v_mfma_f32_32x32x16_f16 v[34:49], v[88:91], v[92:95], v[34:49]
	ds_read_b128 v[124:127], v71
	v_mfma_f32_32x32x16_f16 v[18:33], v[88:91], v[96:99], v[18:33]
	ds_read_b128 v[128:131], v71 offset:4096
	v_mfma_f32_32x32x16_f16 v[2:17], v[88:91], v[100:103], v[2:17]
	ds_read_b128 v[132:135], v71 offset:8192
	s_waitcnt lgkmcnt(0)
	s_barrier
	v_mfma_f32_32x32x16_f16 v[34:49], v[104:107], v[108:111], v[34:49]
	ds_read_b128 v[72:75], v64 offset:28672
	ds_read_b128 v[76:79], v68 offset:28672
	v_mfma_f32_32x32x16_f16 v[18:33], v[104:107], v[112:115], v[18:33]
	ds_read_b128 v[80:83], v68 offset:32768
	ds_read_b128 v[84:87], v68 offset:36864
	v_mfma_f32_32x32x16_f16 v[2:17], v[104:107], v[116:119], v[2:17]
	ds_read_b128 v[88:91], v65 offset:28672
	v_mfma_f32_32x32x16_f16 v[34:49], v[120:123], v[124:127], v[34:49]
	ds_read_b128 v[92:95], v69 offset:28672
	v_mfma_f32_32x32x16_f16 v[18:33], v[120:123], v[128:131], v[18:33]
	ds_read_b128 v[96:99], v69 offset:32768
	v_mfma_f32_32x32x16_f16 v[2:17], v[120:123], v[132:135], v[2:17]
	ds_read_b128 v[100:103], v69 offset:36864
	s_waitcnt lgkmcnt(0)
	v_mfma_f32_32x32x16_f16 v[34:49], v[72:75], v[76:79], v[34:49]
	ds_read_b128 v[104:107], v66 offset:28672
	ds_read_b128 v[108:111], v70 offset:28672
	v_mfma_f32_32x32x16_f16 v[18:33], v[72:75], v[80:83], v[18:33]
	ds_read_b128 v[112:115], v70 offset:32768
	ds_read_b128 v[116:119], v70 offset:36864
	v_mfma_f32_32x32x16_f16 v[2:17], v[72:75], v[84:87], v[2:17]
	ds_read_b128 v[120:123], v67 offset:28672
	v_mfma_f32_32x32x16_f16 v[34:49], v[88:91], v[92:95], v[34:49]
	ds_read_b128 v[124:127], v71 offset:28672
	v_mfma_f32_32x32x16_f16 v[18:33], v[88:91], v[96:99], v[18:33]
	ds_read_b128 v[128:131], v71 offset:32768
	v_mfma_f32_32x32x16_f16 v[2:17], v[88:91], v[100:103], v[2:17]
	ds_read_b128 v[132:135], v71 offset:36864
	s_waitcnt lgkmcnt(0)
	s_barrier
	v_mfma_f32_32x32x16_f16 v[34:49], v[104:107], v[108:111], v[34:49]
	ds_read_b128 v[72:75], v56
	ds_read_b128 v[76:79], v60
	v_mfma_f32_32x32x16_f16 v[18:33], v[104:107], v[112:115], v[18:33]
	ds_read_b128 v[80:83], v60 offset:4096
	ds_read_b128 v[84:87], v60 offset:8192
	v_mfma_f32_32x32x16_f16 v[2:17], v[104:107], v[116:119], v[2:17]
	ds_read_b128 v[88:91], v57
	v_mfma_f32_32x32x16_f16 v[34:49], v[120:123], v[124:127], v[34:49]
	ds_read_b128 v[92:95], v61
	v_mfma_f32_32x32x16_f16 v[18:33], v[120:123], v[128:131], v[18:33]
	ds_read_b128 v[96:99], v61 offset:4096
	v_mfma_f32_32x32x16_f16 v[2:17], v[120:123], v[132:135], v[2:17]
	ds_read_b128 v[100:103], v61 offset:8192
	s_waitcnt lgkmcnt(0)
	v_mfma_f32_32x32x16_f16 v[34:49], v[72:75], v[76:79], v[34:49]
	ds_read_b128 v[104:107], v58
	ds_read_b128 v[108:111], v62
	v_mfma_f32_32x32x16_f16 v[18:33], v[72:75], v[80:83], v[18:33]
	ds_read_b128 v[112:115], v62 offset:4096
	ds_read_b128 v[116:119], v62 offset:8192
	v_mfma_f32_32x32x16_f16 v[2:17], v[72:75], v[84:87], v[2:17]
	ds_read_b128 v[120:123], v59
	v_mfma_f32_32x32x16_f16 v[34:49], v[88:91], v[92:95], v[34:49]
	ds_read_b128 v[124:127], v63
	v_mfma_f32_32x32x16_f16 v[18:33], v[88:91], v[96:99], v[18:33]
	ds_read_b128 v[128:131], v63 offset:4096
	v_mfma_f32_32x32x16_f16 v[2:17], v[88:91], v[100:103], v[2:17]
	ds_read_b128 v[132:135], v63 offset:8192
	s_waitcnt lgkmcnt(0)
	s_barrier
	v_mfma_f32_32x32x16_f16 v[34:49], v[104:107], v[108:111], v[34:49]
	ds_read_b128 v[72:75], v56 offset:28672
	ds_read_b128 v[76:79], v60 offset:28672
	v_mfma_f32_32x32x16_f16 v[18:33], v[104:107], v[112:115], v[18:33]
	ds_read_b128 v[80:83], v60 offset:32768
	ds_read_b128 v[84:87], v60 offset:36864
	v_mfma_f32_32x32x16_f16 v[2:17], v[104:107], v[116:119], v[2:17]
	ds_read_b128 v[88:91], v57 offset:28672
	v_mfma_f32_32x32x16_f16 v[34:49], v[120:123], v[124:127], v[34:49]
	ds_read_b128 v[92:95], v61 offset:28672
	v_mfma_f32_32x32x16_f16 v[18:33], v[120:123], v[128:131], v[18:33]
	ds_read_b128 v[96:99], v61 offset:32768
	v_mfma_f32_32x32x16_f16 v[2:17], v[120:123], v[132:135], v[2:17]
	ds_read_b128 v[100:103], v61 offset:36864
	s_waitcnt lgkmcnt(0)
	v_mfma_f32_32x32x16_f16 v[34:49], v[72:75], v[76:79], v[34:49]
	ds_read_b128 v[104:107], v58 offset:28672
	ds_read_b128 v[108:111], v62 offset:28672
	v_mfma_f32_32x32x16_f16 v[18:33], v[72:75], v[80:83], v[18:33]
	ds_read_b128 v[112:115], v62 offset:32768
	ds_read_b128 v[116:119], v62 offset:36864
	v_mfma_f32_32x32x16_f16 v[2:17], v[72:75], v[84:87], v[2:17]
	ds_read_b128 v[120:123], v59 offset:28672
	v_mfma_f32_32x32x16_f16 v[34:49], v[88:91], v[92:95], v[34:49]
	ds_read_b128 v[124:127], v63 offset:28672
	v_mfma_f32_32x32x16_f16 v[18:33], v[88:91], v[96:99], v[18:33]
	ds_read_b128 v[128:131], v63 offset:32768
	v_mfma_f32_32x32x16_f16 v[2:17], v[88:91], v[100:103], v[2:17]
	ds_read_b128 v[132:135], v63 offset:36864
	s_waitcnt lgkmcnt(0)
	s_barrier
	v_mfma_f32_32x32x16_f16 v[34:49], v[104:107], v[108:111], v[34:49]
	ds_read_b128 v[72:75], v64
	ds_read_b128 v[76:79], v68
	v_mfma_f32_32x32x16_f16 v[18:33], v[104:107], v[112:115], v[18:33]
	ds_read_b128 v[80:83], v68 offset:4096
	ds_read_b128 v[84:87], v68 offset:8192
	v_mfma_f32_32x32x16_f16 v[2:17], v[104:107], v[116:119], v[2:17]
	ds_read_b128 v[88:91], v65
	v_mfma_f32_32x32x16_f16 v[34:49], v[120:123], v[124:127], v[34:49]
	ds_read_b128 v[92:95], v69
	v_mfma_f32_32x32x16_f16 v[18:33], v[120:123], v[128:131], v[18:33]
	ds_read_b128 v[96:99], v69 offset:4096
	v_mfma_f32_32x32x16_f16 v[2:17], v[120:123], v[132:135], v[2:17]
	ds_read_b128 v[100:103], v69 offset:8192
	s_waitcnt lgkmcnt(0)
	v_mfma_f32_32x32x16_f16 v[34:49], v[72:75], v[76:79], v[34:49]
	ds_read_b128 v[104:107], v66
	ds_read_b128 v[108:111], v70
	v_mfma_f32_32x32x16_f16 v[18:33], v[72:75], v[80:83], v[18:33]
	ds_read_b128 v[112:115], v70 offset:4096
	ds_read_b128 v[116:119], v70 offset:8192
	v_mfma_f32_32x32x16_f16 v[2:17], v[72:75], v[84:87], v[2:17]
	ds_read_b128 v[120:123], v67
	v_mfma_f32_32x32x16_f16 v[34:49], v[88:91], v[92:95], v[34:49]
	ds_read_b128 v[124:127], v71
	v_mfma_f32_32x32x16_f16 v[18:33], v[88:91], v[96:99], v[18:33]
	ds_read_b128 v[128:131], v71 offset:4096
	v_mfma_f32_32x32x16_f16 v[2:17], v[88:91], v[100:103], v[2:17]
	ds_read_b128 v[132:135], v71 offset:8192
	s_waitcnt lgkmcnt(0)
	s_barrier
	v_mfma_f32_32x32x16_f16 v[34:49], v[104:107], v[108:111], v[34:49]
	ds_read_b128 v[72:75], v64 offset:28672
	ds_read_b128 v[76:79], v68 offset:28672
	v_mfma_f32_32x32x16_f16 v[18:33], v[104:107], v[112:115], v[18:33]
	ds_read_b128 v[80:83], v68 offset:32768
	ds_read_b128 v[84:87], v68 offset:36864
	v_mfma_f32_32x32x16_f16 v[2:17], v[104:107], v[116:119], v[2:17]
	ds_read_b128 v[88:91], v65 offset:28672
	v_mfma_f32_32x32x16_f16 v[34:49], v[120:123], v[124:127], v[34:49]
	ds_read_b128 v[92:95], v69 offset:28672
	v_mfma_f32_32x32x16_f16 v[18:33], v[120:123], v[128:131], v[18:33]
	ds_read_b128 v[96:99], v69 offset:32768
	v_mfma_f32_32x32x16_f16 v[2:17], v[120:123], v[132:135], v[2:17]
	ds_read_b128 v[100:103], v69 offset:36864
	s_waitcnt lgkmcnt(0)
	v_mfma_f32_32x32x16_f16 v[34:49], v[72:75], v[76:79], v[34:49]
	ds_read_b128 v[104:107], v66 offset:28672
	ds_read_b128 v[108:111], v70 offset:28672
	v_mfma_f32_32x32x16_f16 v[18:33], v[72:75], v[80:83], v[18:33]
	ds_read_b128 v[112:115], v70 offset:32768
	ds_read_b128 v[116:119], v70 offset:36864
	v_mfma_f32_32x32x16_f16 v[2:17], v[72:75], v[84:87], v[2:17]
	ds_read_b128 v[120:123], v67 offset:28672
	v_mfma_f32_32x32x16_f16 v[34:49], v[88:91], v[92:95], v[34:49]
	ds_read_b128 v[124:127], v71 offset:28672
	v_mfma_f32_32x32x16_f16 v[18:33], v[88:91], v[96:99], v[18:33]
	ds_read_b128 v[128:131], v71 offset:32768
	v_mfma_f32_32x32x16_f16 v[2:17], v[88:91], v[100:103], v[2:17]
	ds_read_b128 v[132:135], v71 offset:36864
	s_waitcnt lgkmcnt(0)
	v_mfma_f32_32x32x16_f16 v[34:49], v[104:107], v[108:111], v[34:49]
	v_mfma_f32_32x32x16_f16 v[18:33], v[104:107], v[112:115], v[18:33]
	v_mfma_f32_32x32x16_f16 v[2:17], v[104:107], v[116:119], v[2:17]
	v_mfma_f32_32x32x16_f16 v[34:49], v[120:123], v[124:127], v[34:49]
	v_mfma_f32_32x32x16_f16 v[18:33], v[120:123], v[128:131], v[18:33]
	v_mfma_f32_32x32x16_f16 v[2:17], v[120:123], v[132:135], v[2:17]
	v_add_u32_e32 v51, s9, v51
	v_lshlrev_b32_e32 v104, 2, v51
	global_load_dword v105, v104, s[4:5]
	global_load_dword v106, v104, s[4:5] offset:128
	global_load_dword v107, v104, s[4:5] offset:256
	s_add_i32 s2, s2, s8
	v_lshl_add_u32 v108, v50, 2, s2
	v_mul_u32_u24_e32 v108, 0xc00, v108
	v_add_u32_e32 v108, v108, v104
	s_waitcnt vmcnt(0)
	s_nop 15
	v_add_f32_e32 v110, v105, v34
	v_add_f32_e32 v111, v106, v18
	v_add_f32_e32 v112, v107, v2
	global_store_dword v108, v110, s[6:7] nt
	global_store_dword v108, v111, s[6:7] offset:128 nt
	global_store_dword v108, v112, s[6:7] offset:256 nt
	v_add_u32_e32 v109, 0xc00, v108
	v_add_f32_e32 v110, v105, v35
	v_add_f32_e32 v111, v106, v19
	v_add_f32_e32 v112, v107, v3
	global_store_dword v109, v110, s[6:7] nt
	global_store_dword v109, v111, s[6:7] offset:128 nt
	global_store_dword v109, v112, s[6:7] offset:256 nt
	v_add_u32_e32 v109, 0x1800, v108
	v_add_f32_e32 v110, v105, v36
	v_add_f32_e32 v111, v106, v20
	v_add_f32_e32 v112, v107, v4
	global_store_dword v109, v110, s[6:7] nt
	global_store_dword v109, v111, s[6:7] offset:128 nt
	global_store_dword v109, v112, s[6:7] offset:256 nt
	v_add_u32_e32 v109, 0x2400, v108
	v_add_f32_e32 v110, v105, v37
	v_add_f32_e32 v111, v106, v21
	v_add_f32_e32 v112, v107, v5
	global_store_dword v109, v110, s[6:7] nt
	global_store_dword v109, v111, s[6:7] offset:128 nt
	global_store_dword v109, v112, s[6:7] offset:256 nt
	v_add_u32_e32 v109, 0x6000, v108
	v_add_f32_e32 v110, v105, v38
	v_add_f32_e32 v111, v106, v22
	v_add_f32_e32 v112, v107, v6
	global_store_dword v109, v110, s[6:7] nt
	global_store_dword v109, v111, s[6:7] offset:128 nt
	global_store_dword v109, v112, s[6:7] offset:256 nt
	v_add_u32_e32 v109, 0x6c00, v108
	v_add_f32_e32 v110, v105, v39
	v_add_f32_e32 v111, v106, v23
	v_add_f32_e32 v112, v107, v7
	global_store_dword v109, v110, s[6:7] nt
	global_store_dword v109, v111, s[6:7] offset:128 nt
	global_store_dword v109, v112, s[6:7] offset:256 nt
	v_add_u32_e32 v109, 0x7800, v108
	v_add_f32_e32 v110, v105, v40
	v_add_f32_e32 v111, v106, v24
	v_add_f32_e32 v112, v107, v8
	global_store_dword v109, v110, s[6:7] nt
	global_store_dword v109, v111, s[6:7] offset:128 nt
	global_store_dword v109, v112, s[6:7] offset:256 nt
	v_add_u32_e32 v109, 0x8400, v108
	v_add_f32_e32 v110, v105, v41
	v_add_f32_e32 v111, v106, v25
	v_add_f32_e32 v112, v107, v9
	global_store_dword v109, v110, s[6:7] nt
	global_store_dword v109, v111, s[6:7] offset:128 nt
	global_store_dword v109, v112, s[6:7] offset:256 nt
	v_add_u32_e32 v109, 0xc000, v108
	v_add_f32_e32 v110, v105, v42
	v_add_f32_e32 v111, v106, v26
	v_add_f32_e32 v112, v107, v10
	global_store_dword v109, v110, s[6:7] nt
	global_store_dword v109, v111, s[6:7] offset:128 nt
	global_store_dword v109, v112, s[6:7] offset:256 nt
	v_add_u32_e32 v109, 0xcc00, v108
	v_add_f32_e32 v110, v105, v43
	v_add_f32_e32 v111, v106, v27
	v_add_f32_e32 v112, v107, v11
	global_store_dword v109, v110, s[6:7] nt
	global_store_dword v109, v111, s[6:7] offset:128 nt
	global_store_dword v109, v112, s[6:7] offset:256 nt
	v_add_u32_e32 v109, 0xd800, v108
	v_add_f32_e32 v110, v105, v44
	v_add_f32_e32 v111, v106, v28
	v_add_f32_e32 v112, v107, v12
	global_store_dword v109, v110, s[6:7] nt
	global_store_dword v109, v111, s[6:7] offset:128 nt
	global_store_dword v109, v112, s[6:7] offset:256 nt
	v_add_u32_e32 v109, 0xe400, v108
	v_add_f32_e32 v110, v105, v45
	v_add_f32_e32 v111, v106, v29
	v_add_f32_e32 v112, v107, v13
	global_store_dword v109, v110, s[6:7] nt
	global_store_dword v109, v111, s[6:7] offset:128 nt
	global_store_dword v109, v112, s[6:7] offset:256 nt
	v_add_u32_e32 v109, 0x12000, v108
	v_add_f32_e32 v110, v105, v46
	v_add_f32_e32 v111, v106, v30
	v_add_f32_e32 v112, v107, v14
	global_store_dword v109, v110, s[6:7] nt
	global_store_dword v109, v111, s[6:7] offset:128 nt
	global_store_dword v109, v112, s[6:7] offset:256 nt
	v_add_u32_e32 v109, 0x12c00, v108
	v_add_f32_e32 v110, v105, v47
	v_add_f32_e32 v111, v106, v31
	v_add_f32_e32 v112, v107, v15
	global_store_dword v109, v110, s[6:7] nt
	global_store_dword v109, v111, s[6:7] offset:128 nt
	global_store_dword v109, v112, s[6:7] offset:256 nt
	v_add_u32_e32 v109, 0x13800, v108
	v_add_f32_e32 v110, v105, v48
	v_add_f32_e32 v111, v106, v32
	v_add_f32_e32 v112, v107, v16
	global_store_dword v109, v110, s[6:7] nt
	global_store_dword v109, v111, s[6:7] offset:128 nt
	global_store_dword v109, v112, s[6:7] offset:256 nt
	v_add_u32_e32 v109, 0x14400, v108
	v_add_f32_e32 v110, v105, v49
	v_add_f32_e32 v111, v106, v33
	v_add_f32_e32 v112, v107, v17
	global_store_dword v109, v110, s[6:7] nt
	global_store_dword v109, v111, s[6:7] offset:128 nt
	global_store_dword v109, v112, s[6:7] offset:256 nt
	s_endpgm

	.amdhsa_kernel _Z15out_proj_kernelPKDF16_S0_PKfPf
		.amdhsa_group_segment_fixed_size 0
		.amdhsa_private_segment_fixed_size 0
		.amdhsa_kernarg_size 32
		.amdhsa_user_sgpr_count 2
		.amdhsa_user_sgpr_dispatch_ptr 0
		.amdhsa_user_sgpr_queue_ptr 0
		.amdhsa_user_sgpr_kernarg_segment_ptr 1
		.amdhsa_user_sgpr_dispatch_id 0
		.amdhsa_user_sgpr_kernarg_preload_length 0
		.amdhsa_user_sgpr_kernarg_preload_offset 0
		.amdhsa_user_sgpr_private_segment_size 0
		.amdhsa_uses_dynamic_stack 0
		.amdhsa_enable_private_segment 0
		.amdhsa_system_sgpr_workgroup_id_x 1
		.amdhsa_system_sgpr_workgroup_id_y 0
		.amdhsa_system_sgpr_workgroup_id_z 0
		.amdhsa_system_sgpr_workgroup_info 0
		.amdhsa_system_vgpr_workitem_id 0
		.amdhsa_next_free_vgpr 136
		.amdhsa_next_free_sgpr 61
		.amdhsa_accum_offset 136
		.amdhsa_reserve_vcc 1
		.amdhsa_float_round_mode_32 0
		.amdhsa_float_round_mode_16_64 0
		.amdhsa_float_denorm_mode_32 3
		.amdhsa_float_denorm_mode_16_64 3
		.amdhsa_dx10_clamp 1
		.amdhsa_ieee_mode 1
		.amdhsa_fp16_overflow 0
		.amdhsa_tg_split 0
		.amdhsa_exception_fp_ieee_invalid_op 0
		.amdhsa_exception_fp_denorm_src 0
		.amdhsa_exception_fp_ieee_div_zero 0
		.amdhsa_exception_fp_ieee_overflow 0
		.amdhsa_exception_fp_ieee_underflow 0
		.amdhsa_exception_fp_ieee_inexact 0
		.amdhsa_exception_int_div_zero 0
	.end_amdhsa_kernel

amdhsa.kernels:
  - .agpr_count:     0
    .args:
      - .actual_access:  read_only
        .address_space:  global
        .offset:         0
        .size:           8
        .value_kind:     global_buffer
      - .actual_access:  read_only
        .address_space:  global
        .offset:         8
        .size:           8
        .value_kind:     global_buffer
      - .actual_access:  read_only
        .address_space:  global
        .offset:         16
        .size:           8
        .value_kind:     global_buffer
      - .actual_access:  read_only
        .address_space:  global
        .offset:         24
        .size:           8
        .value_kind:     global_buffer
      - .actual_access:  read_only
        .address_space:  global
        .offset:         32
        .size:           8
        .value_kind:     global_buffer
      - .actual_access:  read_only
        .address_space:  global
        .offset:         40
        .size:           8
        .value_kind:     global_buffer
      - .actual_access:  read_only
        .address_space:  global
        .offset:         48
        .size:           8
        .value_kind:     global_buffer
      - .actual_access:  write_only
        .address_space:  global
        .offset:         56
        .size:           8
        .value_kind:     global_buffer
      - .actual_access:  write_only
        .address_space:  global
        .offset:         64
        .size:           8
        .value_kind:     global_buffer
    .group_segment_fixed_size: 0
    .kernarg_segment_align: 8
    .kernarg_segment_size: 72
    .language:       OpenCL C
    .language_version:
      - 2
      - 0
    .max_flat_workgroup_size: 256
    .name:           _Z11prep_kernelPKfS0_S0_S0_S0_S0_S0_PDF16_S1_
    .private_segment_fixed_size: 0
    .sgpr_count:     21
    .sgpr_spill_count: 0
    .symbol:         _Z11prep_kernelPKfS0_S0_S0_S0_S0_S0_PDF16_S1_.kd
    .uniform_work_group_size: 1
    .uses_dynamic_stack: false
    .vgpr_count:     10
    .vgpr_spill_count: 0
    .wavefront_size: 64
  - .agpr_count:     0
    .args:
      - .address_space:  global
        .offset:         0
        .size:           8
        .value_kind:     global_buffer
      - .address_space:  global
        .offset:         8
        .size:           8
        .value_kind:     global_buffer
      - .actual_access:  read_only
        .address_space:  global
        .offset:         16
        .size:           8
        .value_kind:     global_buffer
      - .actual_access:  read_only
        .address_space:  global
        .offset:         24
        .size:           8
        .value_kind:     global_buffer
      - .actual_access:  read_only
        .address_space:  global
        .offset:         32
        .size:           8
        .value_kind:     global_buffer
      - .actual_access:  write_only
        .address_space:  global
        .offset:         40
        .size:           8
        .value_kind:     global_buffer
      - .actual_access:  write_only
        .address_space:  global
        .offset:         48
        .size:           8
        .value_kind:     global_buffer
      - .actual_access:  write_only
        .address_space:  global
        .offset:         56
        .size:           8
        .value_kind:     global_buffer
    .group_segment_fixed_size: 0
    .kernarg_segment_align: 8
    .kernarg_segment_size: 64
    .language:       OpenCL C
    .language_version:
      - 2
      - 0
    .max_flat_workgroup_size: 768
    .name:           _Z15qkv_proj_kernelPKDF16_S0_PKfS2_S2_PDF16_S3_S3_
    .private_segment_fixed_size: 0
    .sgpr_count:     47
    .sgpr_spill_count: 0
    .symbol:         _Z15qkv_proj_kernelPKDF16_S0_PKfS2_S2_PDF16_S3_S3_.kd
    .uniform_work_group_size: 1
    .uses_dynamic_stack: false
    .vgpr_count:     152
    .vgpr_spill_count: 0
    .wavefront_size: 64
  - .agpr_count:     0
    .args:
      - .address_space:  global
        .offset:         0
        .size:           8
        .value_kind:     global_buffer
      - .address_space:  global
        .offset:         8
        .size:           8
        .value_kind:     global_buffer
      - .actual_access:  read_only
        .address_space:  global
        .offset:         16
        .size:           8
        .value_kind:     global_buffer
      - .actual_access:  write_only
        .address_space:  global
        .offset:         24
        .size:           8
        .value_kind:     global_buffer
    .group_segment_fixed_size: 0
    .kernarg_segment_align: 8
    .kernarg_segment_size: 32
    .language:       OpenCL C
    .language_version:
      - 2
      - 0
    .max_flat_workgroup_size: 384
    .name:           _Z15out_proj_kernelPKDF16_S0_PKfPf
    .private_segment_fixed_size: 0
    .sgpr_count:     67
    .sgpr_spill_count: 0
    .symbol:         _Z15out_proj_kernelPKDF16_S0_PKfPf.kd
    .uniform_work_group_size: 1
    .uses_dynamic_stack: false
    .vgpr_count:     136
    .vgpr_spill_count: 0
    .wavefront_size: 64
  - .agpr_count:     0
    .args:
      - .actual_access:  read_only
        .address_space:  global
        .offset:         0
        .size:           8
        .value_kind:     global_buffer
      - .address_space:  global
        .offset:         8
        .size:           8
        .value_kind:     global_buffer
      - .address_space:  global
        .offset:         16
        .size:           8
        .value_kind:     global_buffer
      - .actual_access:  write_only
        .address_space:  global
        .offset:         24
        .size:           8
        .value_kind:     global_buffer
      - .actual_access:  write_only
        .address_space:  global
        .offset:         32
        .size:           8
        .value_kind:     global_buffer
    .group_segment_fixed_size: 49152
    .kernarg_segment_align: 8
    .kernarg_segment_size: 40
    .language:       OpenCL C
    .language_version:
      - 2
      - 0
    .max_flat_workgroup_size: 256
    .name:           _Z11attn_kernelPKDF16_S0_S0_PDF16_P15HIP_vector_typeIfLj2EE
    .private_segment_fixed_size: 0
    .sgpr_count:     34
    .sgpr_spill_count: 0
    .symbol:         _Z11attn_kernelPKDF16_S0_S0_PDF16_P15HIP_vector_typeIfLj2EE.kd
    .uniform_work_group_size: 1
    .uses_dynamic_stack: false
    .vgpr_count:     145
    .vgpr_spill_count: 0
    .wavefront_size: 64
  - .agpr_count:     0
    .args:
      - .actual_access:  read_only
        .address_space:  global
        .offset:         0
        .size:           8
        .value_kind:     global_buffer
      - .actual_access:  read_only
        .address_space:  global
        .offset:         8
        .size:           8
        .value_kind:     global_buffer
      - .actual_access:  write_only
        .address_space:  global
        .offset:         16
        .size:           8
        .value_kind:     global_buffer
    .group_segment_fixed_size: 0
    .kernarg_segment_align: 8
    .kernarg_segment_size: 24
    .language:       OpenCL C
    .language_version:
      - 2
      - 0
    .max_flat_workgroup_size: 256
    .name:           _Z14combine_kernelPKDF16_PK15HIP_vector_typeIfLj2EEPDF16_
    .private_segment_fixed_size: 0
    .sgpr_count:     16
    .sgpr_spill_count: 0
    .symbol:         _Z14combine_kernelPKDF16_PK15HIP_vector_typeIfLj2EEPDF16_.kd
    .uniform_work_group_size: 1
    .uses_dynamic_stack: false
    .vgpr_count:     44
    .vgpr_spill_count: 0
    .wavefront_size: 64
